# strategy 4 setprio A/B: v32 with every s_setprio in the four GEMM K-loops deleted (no priority flips at all)
# speedup vs baseline: 1.0054x; 1.0053x over previous
; #define PG8_STAGE(bufoff, gbase, voff) do { _Pragma("unroll") for (int _i = 0; _i < 2; ++_i) \
;         __builtin_amdgcn_global_load_lds((const unsigned*)((const char*)(gbase) + (voff)[_i]), (LAS unsigned*)(lds + (bufoff) + ldsw + _i * 8192), 16, 0, 0); } while (0)
; #define PG8_LDA(dst, b, h) do { _Pragma("unroll") for (int m = 0; m < 4; ++m) _Pragma("unroll") for (int k = 0; k < 2; ++k) dst[m][k] = *(const LAS bf16x8*)(lds + PG8_SA(b, h) + aoff + m * 2048 + k * 1024); } while (0)
; #define PG8_LDB(dst, b, h) do { _Pragma("unroll") for (int n = 0; n < 2; ++n) _Pragma("unroll") for (int k = 0; k < 2; ++k) dst[n][k] = *(const LAS bf16x8*)(lds + PG8_SB(b, h) + boff + n * 2048 + k * 1024); } while (0)
; #define PG8_MMA(ai, bj, At, Bt) do { __builtin_amdgcn_s_setprio(1); _Pragma("unroll") for (int m = 0; m < 4; ++m) _Pragma("unroll") for (int n = 0; n < 2; ++n) _Pragma("unroll") for (int k = 0; k < 2; ++k) \
;         acc[ai][bj][m][n] = __builtin_amdgcn_mfma_f32_16x16x32_bf16(Bt[n][k], At[m][k], acc[ai][bj][m][n], 0, 0, 0); __builtin_amdgcn_s_setprio(0); } while (0)
; #define PG8_WAIT_V(n) asm volatile("s_waitcnt vmcnt(" #n ")" ::: "memory")
; #define PG8_WAIT_L(n) asm volatile("s_waitcnt lgkmcnt(" #n ")" ::: "memory")
; #define PG8_BAR __builtin_amdgcn_s_barrier()
; #define PG8_SCHED __builtin_amdgcn_sched_barrier(0)
; #define PG8_WAIT_V(n) asm volatile("s_waitcnt vmcnt(" #n ")" ::: "memory")
; #define PG8_WAIT_L(n) asm volatile("s_waitcnt lgkmcnt(" #n ")" ::: "memory")
;     ...
;         for (int t = 0; t < nt; t += 2) {
;             const bool last = (t == nt - 2);
;             const char* a1 = cA + (size_t)(t + 1) * kstepA;
;             const char* a2 = last ? nA : cA + (size_t)(t + 2) * kstepA; const char* b2 = last ? nB : cB + (size_t)(t + 2) * kstep;
;             const char* a3 = a2 + kstepA; const char* b3 = b2 + kstep;
;             PG8_LDB(B0, 0, 0); PG8_LDB(B1, 0, 1); PG8_SCHED; PG8_LDA(At, 0, 0); PG8_STAGE(PG8_SA(1, 1), a1 + hstepA, voffA);
;             PG8_WAIT_V(8); PG8_WAIT_L(0); PG8_BAR; PG8_MMA(0, 0, At, B0); PG8_MMA(0, 1, At, B1); PG8_BAR; PG8_SCHED;
;             PG8_LDA(At, 0, 1); PG8_STAGE(PG8_SB(0, 0), b2, voffB); PG8_STAGE(PG8_SB(0, 1), b2 + hstep, voffB); PG8_STAGE(PG8_SA(0, 0), a2, voffA);
;             PG8_WAIT_V(8); PG8_WAIT_L(0); PG8_BAR; if (hi_on) { PG8_MMA(1, 0, At, B0); PG8_MMA(1, 1, At, B1); } PG8_BAR; PG8_SCHED;
.LBB0_213:
	s_add_u32 s22, s6, 0xfffc0080
	s_addc_u32 s23, s7, -1
	s_add_i32 s27, 0, 0x10000
	s_cmp_eq_u32 s26, 12
	s_cselect_b32 s25, s19, s23
	s_cselect_b32 s24, s18, s22
	v_add_u32_e32 v52, s27, v1
	s_cselect_b32 s23, s21, s17
	s_cselect_b32 s22, s20, s15
	s_add_i32 s42, 0, 0x14000
	ds_read_b128 v[62:65], v52
	ds_read_b128 v[66:69], v52 offset:1024
	ds_read_b128 v[156:159], v52 offset:2048
	ds_read_b128 v[160:163], v52 offset:3072
	v_add_u32_e32 v52, s42, v1
	ds_read_b128 v[168:171], v52
	ds_read_b128 v[172:175], v52 offset:1024
	ds_read_b128 v[176:179], v52 offset:2048
	ds_read_b128 v[180:183], v52 offset:3072
	v_lshl_add_u64 v[52:53], s[6:7], 0, v[152:153]
	s_add_i32 m0, s30, 0xc000
	ds_read_b128 v[184:187], v166
	ds_read_b128 v[188:191], v166 offset:1024
	ds_read_b128 v[192:195], v166 offset:2048
	ds_read_b128 v[204:207], v166 offset:3072
	ds_read_b128 v[208:211], v166 offset:4096
	ds_read_b128 v[212:215], v166 offset:5120
	ds_read_b128 v[216:219], v166 offset:6144
	ds_read_b128 v[220:223], v166 offset:7168
	global_load_lds_dwordx4 v[52:53], off
	v_lshl_add_u64 v[52:53], s[6:7], 0, v[154:155]
	s_add_i32 m0, s30, 0xe000
	s_nop 0
	global_load_lds_dwordx4 v[52:53], off
	s_waitcnt vmcnt(8)
	s_waitcnt lgkmcnt(0)
	s_barrier
	s_waitcnt lgkmcnt(0)
	v_mfma_f32_16x16x32_bf16 v[138:141], v[62:65], v[184:187], v[138:141]
	v_mfma_f32_16x16x32_bf16 v[134:137], v[156:159], v[184:187], v[134:137]
	v_mfma_f32_16x16x32_bf16 v[122:125], v[62:65], v[192:195], v[122:125]
	v_mfma_f32_16x16x32_bf16 v[118:121], v[156:159], v[192:195], v[118:121]
	v_mfma_f32_16x16x32_bf16 v[106:109], v[62:65], v[208:211], v[106:109]
	v_mfma_f32_16x16x32_bf16 v[102:105], v[156:159], v[208:211], v[102:105]
	v_mfma_f32_16x16x32_bf16 v[90:93], v[62:65], v[216:219], v[90:93]
	v_mfma_f32_16x16x32_bf16 v[86:89], v[156:159], v[216:219], v[86:89]
	v_mfma_f32_16x16x32_bf16 v[138:141], v[66:69], v[188:191], v[138:141]
	v_mfma_f32_16x16x32_bf16 v[134:137], v[160:163], v[188:191], v[134:137]
	v_mfma_f32_16x16x32_bf16 v[122:125], v[66:69], v[204:207], v[122:125]
	v_mfma_f32_16x16x32_bf16 v[118:121], v[160:163], v[204:207], v[118:121]
	v_mfma_f32_16x16x32_bf16 v[106:109], v[66:69], v[212:215], v[106:109]
	v_mfma_f32_16x16x32_bf16 v[102:105], v[160:163], v[212:215], v[102:105]
	v_mfma_f32_16x16x32_bf16 v[90:93], v[66:69], v[220:223], v[90:93]
	v_mfma_f32_16x16x32_bf16 v[86:89], v[160:163], v[220:223], v[86:89]
	v_mfma_f32_16x16x32_bf16 v[130:133], v[168:171], v[184:187], v[130:133]
	v_mfma_f32_16x16x32_bf16 v[126:129], v[176:179], v[184:187], v[126:129]
	v_mfma_f32_16x16x32_bf16 v[114:117], v[168:171], v[192:195], v[114:117]
	v_mfma_f32_16x16x32_bf16 v[110:113], v[176:179], v[192:195], v[110:113]
	v_mfma_f32_16x16x32_bf16 v[98:101], v[168:171], v[208:211], v[98:101]
	v_mfma_f32_16x16x32_bf16 v[94:97], v[176:179], v[208:211], v[94:97]
	v_mfma_f32_16x16x32_bf16 v[82:85], v[168:171], v[216:219], v[82:85]
	v_mfma_f32_16x16x32_bf16 v[78:81], v[176:179], v[216:219], v[78:81]
	v_mfma_f32_16x16x32_bf16 v[130:133], v[172:175], v[188:191], v[130:133]
	v_mfma_f32_16x16x32_bf16 v[126:129], v[180:183], v[188:191], v[126:129]
	v_mfma_f32_16x16x32_bf16 v[114:117], v[172:175], v[204:207], v[114:117]
	v_mfma_f32_16x16x32_bf16 v[110:113], v[180:183], v[204:207], v[110:113]
	v_mfma_f32_16x16x32_bf16 v[98:101], v[172:175], v[212:215], v[98:101]
	v_mfma_f32_16x16x32_bf16 v[94:97], v[180:183], v[212:215], v[94:97]
	v_mfma_f32_16x16x32_bf16 v[82:85], v[172:175], v[220:223], v[82:85]
	v_mfma_f32_16x16x32_bf16 v[78:81], v[180:183], v[220:223], v[78:81]
	s_barrier
	s_add_i32 s27, s27, s29
	v_lshl_add_u64 v[196:197], s[22:23], 0, v[144:145]
	s_mov_b32 m0, s27
	ds_read_b128 v[184:187], v166 offset:16384
	ds_read_b128 v[188:191], v166 offset:17408
	ds_read_b128 v[192:195], v166 offset:18432
	ds_read_b128 v[204:207], v166 offset:19456
	ds_read_b128 v[208:211], v166 offset:20480
	ds_read_b128 v[212:215], v166 offset:21504
	ds_read_b128 v[216:219], v166 offset:22528
	ds_read_b128 v[220:223], v166 offset:23552
	global_load_lds_dwordx4 v[196:197], off
	s_add_i32 m0, s27, 0x2000
	s_add_u32 s36, s22, 0x40000
	v_lshl_add_u64 v[224:225], s[22:23], 0, v[148:149]
	s_addc_u32 s37, s23, 0
	s_add_i32 s27, s42, s29
	global_load_lds_dwordx4 v[224:225], off
	v_lshl_add_u64 v[52:53], s[36:37], 0, v[144:145]
	s_mov_b32 m0, s27
	v_lshl_add_u64 v[226:227], s[24:25], 0, v[142:143]
	global_load_lds_dwordx4 v[52:53], off
	v_lshl_add_u64 v[52:53], s[36:37], 0, v[148:149]
	s_add_i32 m0, s27, 0x2000
	v_lshl_add_u64 v[228:229], s[24:25], 0, v[146:147]
	global_load_lds_dwordx4 v[52:53], off
	s_mov_b32 m0, s30
	s_nop 0
	global_load_lds_dwordx4 v[226:227], off
	s_mov_b32 m0, s31
	s_nop 0
	global_load_lds_dwordx4 v[228:229], off
	s_waitcnt vmcnt(8)
	s_waitcnt lgkmcnt(0)
	s_barrier
; #define PG8_STAGE(bufoff, gbase, voff) do { _Pragma("unroll") for (int _i = 0; _i < 2; ++_i) \
;         __builtin_amdgcn_global_load_lds((const unsigned*)((const char*)(gbase) + (voff)[_i]), (LAS unsigned*)(lds + (bufoff) + ldsw + _i * 8192), 16, 0, 0); } while (0)
; #define PG8_LDA(dst, b, h) do { _Pragma("unroll") for (int m = 0; m < 4; ++m) _Pragma("unroll") for (int k = 0; k < 2; ++k) dst[m][k] = *(const LAS bf16x8*)(lds + PG8_SA(b, h) + aoff + m * 2048 + k * 1024); } while (0)
; #define PG8_LDB(dst, b, h) do { _Pragma("unroll") for (int n = 0; n < 2; ++n) _Pragma("unroll") for (int k = 0; k < 2; ++k) dst[n][k] = *(const LAS bf16x8*)(lds + PG8_SB(b, h) + boff + n * 2048 + k * 1024); } while (0)
; #define PG8_MMA(ai, bj, At, Bt) do { __builtin_amdgcn_s_setprio(1); _Pragma("unroll") for (int m = 0; m < 4; ++m) _Pragma("unroll") for (int n = 0; n < 2; ++n) _Pragma("unroll") for (int k = 0; k < 2; ++k) \
;         acc[ai][bj][m][n] = __builtin_amdgcn_mfma_f32_16x16x32_bf16(Bt[n][k], At[m][k], acc[ai][bj][m][n], 0, 0, 0); __builtin_amdgcn_s_setprio(0); } while (0)
; #define PG8_WAIT_V(n) asm volatile("s_waitcnt vmcnt(" #n ")" ::: "memory")
; #define PG8_WAIT_L(n) asm volatile("s_waitcnt lgkmcnt(" #n ")" ::: "memory")
; #define PG8_BAR __builtin_amdgcn_s_barrier()
; #define PG8_SCHED __builtin_amdgcn_sched_barrier(0)
; #define PG8_STAGE(bufoff, gbase, voff) do { _Pragma("unroll") for (int _i = 0; _i < 2; ++_i) \
;         __builtin_amdgcn_global_load_lds((const unsigned*)((const char*)(gbase) + (voff)[_i]), (LAS unsigned*)(lds + (bufoff) + ldsw + _i * 8192), 16, 0, 0); } while (0)
; #define PG8_LDA(dst, b, h) do { _Pragma("unroll") for (int m = 0; m < 4; ++m) _Pragma("unroll") for (int k = 0; k < 2; ++k) dst[m][k] = *(const LAS bf16x8*)(lds + PG8_SA(b, h) + aoff + m * 2048 + k * 1024); } while (0)
; #define PG8_WAIT_V(n) asm volatile("s_waitcnt vmcnt(" #n ")" ::: "memory")
; #define PG8_WAIT_L(n) asm volatile("s_waitcnt lgkmcnt(" #n ")" ::: "memory")
;     ...
;             PG8_WAIT_V(8); PG8_WAIT_L(0); PG8_BAR; if (hi_on) { PG8_MMA(1, 0, At, B0); PG8_MMA(1, 1, At, B1); } PG8_BAR; PG8_SCHED;
;             PG8_LDB(B0, 1, 0); PG8_LDB(B1, 1, 1); PG8_SCHED; PG8_LDA(At, 1, 0); PG8_STAGE(PG8_SA(0, 1), a2 + hstepA, voffA);
;             PG8_WAIT_V(8); PG8_WAIT_L(0); PG8_BAR; PG8_MMA(0, 0, At, B0); PG8_MMA(0, 1, At, B1); PG8_BAR; PG8_SCHED;
	s_waitcnt lgkmcnt(0)
	v_mfma_f32_16x16x32_bf16 v[74:77], v[62:65], v[184:187], v[74:77]
	v_mfma_f32_16x16x32_bf16 v[70:73], v[156:159], v[184:187], v[70:73]
	v_mfma_f32_16x16x32_bf16 v[48:51], v[62:65], v[192:195], v[48:51]
	v_mfma_f32_16x16x32_bf16 v[44:47], v[156:159], v[192:195], v[44:47]
	v_mfma_f32_16x16x32_bf16 v[30:33], v[62:65], v[208:211], v[30:33]
	v_mfma_f32_16x16x32_bf16 v[26:29], v[156:159], v[208:211], v[26:29]
	v_mfma_f32_16x16x32_bf16 v[14:17], v[62:65], v[216:219], v[14:17]
	v_mfma_f32_16x16x32_bf16 v[10:13], v[156:159], v[216:219], v[10:13]
	v_mfma_f32_16x16x32_bf16 v[74:77], v[66:69], v[188:191], v[74:77]
	v_mfma_f32_16x16x32_bf16 v[70:73], v[160:163], v[188:191], v[70:73]
	v_mfma_f32_16x16x32_bf16 v[48:51], v[66:69], v[204:207], v[48:51]
	v_mfma_f32_16x16x32_bf16 v[44:47], v[160:163], v[204:207], v[44:47]
	v_mfma_f32_16x16x32_bf16 v[30:33], v[66:69], v[212:215], v[30:33]
	v_mfma_f32_16x16x32_bf16 v[26:29], v[160:163], v[212:215], v[26:29]
	v_mfma_f32_16x16x32_bf16 v[14:17], v[66:69], v[220:223], v[14:17]
	v_mfma_f32_16x16x32_bf16 v[10:13], v[160:163], v[220:223], v[10:13]
	v_mfma_f32_16x16x32_bf16 v[58:61], v[168:171], v[184:187], v[58:61]
	v_mfma_f32_16x16x32_bf16 v[52:55], v[176:179], v[184:187], v[54:57]
	v_mfma_f32_16x16x32_bf16 v[40:43], v[168:171], v[192:195], v[40:43]
	v_mfma_f32_16x16x32_bf16 v[36:39], v[176:179], v[192:195], v[36:39]
	v_mfma_f32_16x16x32_bf16 v[22:25], v[168:171], v[208:211], v[22:25]
	v_mfma_f32_16x16x32_bf16 v[18:21], v[176:179], v[208:211], v[18:21]
	v_mfma_f32_16x16x32_bf16 v[6:9], v[168:171], v[216:219], v[6:9]
	v_mfma_f32_16x16x32_bf16 v[2:5], v[176:179], v[216:219], v[2:5]
	v_mfma_f32_16x16x32_bf16 v[58:61], v[172:175], v[188:191], v[58:61]
	v_mfma_f32_16x16x32_bf16 v[52:55], v[180:183], v[188:191], v[52:55]
	v_mfma_f32_16x16x32_bf16 v[40:43], v[172:175], v[204:207], v[40:43]
	v_mfma_f32_16x16x32_bf16 v[36:39], v[180:183], v[204:207], v[36:39]
	v_mfma_f32_16x16x32_bf16 v[22:25], v[172:175], v[212:215], v[22:25]
	v_mfma_f32_16x16x32_bf16 v[18:21], v[180:183], v[212:215], v[18:21]
	v_mfma_f32_16x16x32_bf16 v[6:9], v[172:175], v[220:223], v[6:9]
	v_mfma_f32_16x16x32_bf16 v[2:5], v[180:183], v[220:223], v[2:5]
	s_barrier
	s_add_i32 s27, 0, 0x18000
	v_add_u32_e32 v56, s27, v1
	s_add_i32 s36, 0, 0x1c000
	ds_read_b128 v[62:65], v56
	ds_read_b128 v[66:69], v56 offset:1024
	ds_read_b128 v[156:159], v56 offset:2048
	ds_read_b128 v[160:163], v56 offset:3072
	v_add_u32_e32 v56, s36, v1
	ds_read_b128 v[168:171], v56
	ds_read_b128 v[172:175], v56 offset:1024
	ds_read_b128 v[176:179], v56 offset:2048
	ds_read_b128 v[180:183], v56 offset:3072
	s_add_u32 s24, s24, 0x40000
	s_addc_u32 s25, s25, 0
	s_mov_b32 m0, s34
	v_lshl_add_u64 v[56:57], s[24:25], 0, v[142:143]
	ds_read_b128 v[184:187], v166 offset:32768
	ds_read_b128 v[188:191], v166 offset:33792
	ds_read_b128 v[192:195], v166 offset:34816
	ds_read_b128 v[204:207], v166 offset:35840
	ds_read_b128 v[208:211], v166 offset:36864
	ds_read_b128 v[212:215], v166 offset:37888
	ds_read_b128 v[216:219], v166 offset:38912
	ds_read_b128 v[220:223], v166 offset:39936
	global_load_lds_dwordx4 v[56:57], off
	v_lshl_add_u64 v[56:57], s[24:25], 0, v[146:147]
	s_mov_b32 m0, s35
	s_nop 0
	global_load_lds_dwordx4 v[56:57], off
	s_waitcnt vmcnt(8)
	s_waitcnt lgkmcnt(0)
	s_barrier
	s_waitcnt lgkmcnt(0)
	v_mfma_f32_16x16x32_bf16 v[138:141], v[62:65], v[184:187], v[138:141]
	v_mfma_f32_16x16x32_bf16 v[134:137], v[156:159], v[184:187], v[134:137]
	v_mfma_f32_16x16x32_bf16 v[122:125], v[62:65], v[192:195], v[122:125]
	v_mfma_f32_16x16x32_bf16 v[118:121], v[156:159], v[192:195], v[118:121]
	v_mfma_f32_16x16x32_bf16 v[106:109], v[62:65], v[208:211], v[106:109]
	v_mfma_f32_16x16x32_bf16 v[102:105], v[156:159], v[208:211], v[102:105]
	v_mfma_f32_16x16x32_bf16 v[90:93], v[62:65], v[216:219], v[90:93]
	v_mfma_f32_16x16x32_bf16 v[86:89], v[156:159], v[216:219], v[86:89]
	v_mfma_f32_16x16x32_bf16 v[138:141], v[66:69], v[188:191], v[138:141]
	v_mfma_f32_16x16x32_bf16 v[134:137], v[160:163], v[188:191], v[134:137]
	v_mfma_f32_16x16x32_bf16 v[122:125], v[66:69], v[204:207], v[122:125]
	v_mfma_f32_16x16x32_bf16 v[118:121], v[160:163], v[204:207], v[118:121]
	v_mfma_f32_16x16x32_bf16 v[106:109], v[66:69], v[212:215], v[106:109]
	v_mfma_f32_16x16x32_bf16 v[102:105], v[160:163], v[212:215], v[102:105]
	v_mfma_f32_16x16x32_bf16 v[90:93], v[66:69], v[220:223], v[90:93]
	v_mfma_f32_16x16x32_bf16 v[86:89], v[160:163], v[220:223], v[86:89]
	v_mfma_f32_16x16x32_bf16 v[130:133], v[168:171], v[184:187], v[130:133]
	v_mfma_f32_16x16x32_bf16 v[126:129], v[176:179], v[184:187], v[126:129]
	v_mfma_f32_16x16x32_bf16 v[114:117], v[168:171], v[192:195], v[114:117]
	v_mfma_f32_16x16x32_bf16 v[110:113], v[176:179], v[192:195], v[110:113]
	v_mfma_f32_16x16x32_bf16 v[98:101], v[168:171], v[208:211], v[98:101]
	v_mfma_f32_16x16x32_bf16 v[94:97], v[176:179], v[208:211], v[94:97]
	v_mfma_f32_16x16x32_bf16 v[82:85], v[168:171], v[216:219], v[82:85]
	v_mfma_f32_16x16x32_bf16 v[78:81], v[176:179], v[216:219], v[78:81]
	v_mfma_f32_16x16x32_bf16 v[130:133], v[172:175], v[188:191], v[130:133]
	v_mfma_f32_16x16x32_bf16 v[126:129], v[180:183], v[188:191], v[126:129]
	v_mfma_f32_16x16x32_bf16 v[114:117], v[172:175], v[204:207], v[114:117]
	v_mfma_f32_16x16x32_bf16 v[110:113], v[180:183], v[204:207], v[110:113]
	v_mfma_f32_16x16x32_bf16 v[98:101], v[172:175], v[212:215], v[98:101]
	v_mfma_f32_16x16x32_bf16 v[94:97], v[180:183], v[212:215], v[94:97]
	v_mfma_f32_16x16x32_bf16 v[82:85], v[172:175], v[220:223], v[82:85]
	v_mfma_f32_16x16x32_bf16 v[78:81], v[180:183], v[220:223], v[78:81]
	s_barrier
; #define PG8_STAGE(bufoff, gbase, voff) do { _Pragma("unroll") for (int _i = 0; _i < 2; ++_i) \
;         __builtin_amdgcn_global_load_lds((const unsigned*)((const char*)(gbase) + (voff)[_i]), (LAS unsigned*)(lds + (bufoff) + ldsw + _i * 8192), 16, 0, 0); } while (0)
; #define PG8_LDA(dst, b, h) do { _Pragma("unroll") for (int m = 0; m < 4; ++m) _Pragma("unroll") for (int k = 0; k < 2; ++k) dst[m][k] = *(const LAS bf16x8*)(lds + PG8_SA(b, h) + aoff + m * 2048 + k * 1024); } while (0)
; #define PG8_MMA(ai, bj, At, Bt) do { __builtin_amdgcn_s_setprio(1); _Pragma("unroll") for (int m = 0; m < 4; ++m) _Pragma("unroll") for (int n = 0; n < 2; ++n) _Pragma("unroll") for (int k = 0; k < 2; ++k) \
;         acc[ai][bj][m][n] = __builtin_amdgcn_mfma_f32_16x16x32_bf16(Bt[n][k], At[m][k], acc[ai][bj][m][n], 0, 0, 0); __builtin_amdgcn_s_setprio(0); } while (0)
; #define PG8_WAIT_V(n) asm volatile("s_waitcnt vmcnt(" #n ")" ::: "memory")
; #define PG8_WAIT_L(n) asm volatile("s_waitcnt lgkmcnt(" #n ")" ::: "memory")
; #define PG8_BAR __builtin_amdgcn_s_barrier()
; #define PG8_SCHED __builtin_amdgcn_sched_barrier(0)
; #define PG8_STAGE(bufoff, gbase, voff) do { _Pragma("unroll") for (int _i = 0; _i < 2; ++_i) \
;         __builtin_amdgcn_global_load_lds((const unsigned*)((const char*)(gbase) + (voff)[_i]), (LAS unsigned*)(lds + (bufoff) + ldsw + _i * 8192), 16, 0, 0); } while (0)
; #define PG8_LDA(dst, b, h) do { _Pragma("unroll") for (int m = 0; m < 4; ++m) _Pragma("unroll") for (int k = 0; k < 2; ++k) dst[m][k] = *(const LAS bf16x8*)(lds + PG8_SA(b, h) + aoff + m * 2048 + k * 1024); } while (0)
; #define PG8_MMA(ai, bj, At, Bt) do { __builtin_amdgcn_s_setprio(1); _Pragma("unroll") for (int m = 0; m < 4; ++m) _Pragma("unroll") for (int n = 0; n < 2; ++n) _Pragma("unroll") for (int k = 0; k < 2; ++k) \
;         acc[ai][bj][m][n] = __builtin_amdgcn_mfma_f32_16x16x32_bf16(Bt[n][k], At[m][k], acc[ai][bj][m][n], 0, 0, 0); __builtin_amdgcn_s_setprio(0); } while (0)
; #define PG8_WAIT_V(n) asm volatile("s_waitcnt vmcnt(" #n ")" ::: "memory")
;     ...
;             PG8_LDA(At, 1, 1); PG8_STAGE(PG8_SB(1, 0), b3, voffB); PG8_STAGE(PG8_SB(1, 1), b3 + hstep, voffB); PG8_STAGE(PG8_SA(1, 0), a3, voffA);
;             PG8_WAIT_V(8); PG8_WAIT_L(0); PG8_BAR; if (hi_on) { PG8_MMA(1, 0, At, B0); PG8_MMA(1, 1, At, B1); } PG8_BAR; PG8_SCHED;
;         }
;         if (wr == 0) PG8_BAR;
	s_add_i32 s24, s27, s29
	v_lshl_add_u64 v[56:57], v[196:197], 0, s[88:89]
	s_mov_b32 m0, s24
	ds_read_b128 v[184:187], v166 offset:49152
	ds_read_b128 v[188:191], v166 offset:50176
	ds_read_b128 v[192:195], v166 offset:51200
	ds_read_b128 v[204:207], v166 offset:52224
	ds_read_b128 v[208:211], v166 offset:53248
	ds_read_b128 v[212:215], v166 offset:54272
	ds_read_b128 v[216:219], v166 offset:55296
	ds_read_b128 v[220:223], v166 offset:56320
	global_load_lds_dwordx4 v[56:57], off
	s_add_i32 m0, s24, 0x2000
	s_add_u32 s22, s22, 0x40080
	v_lshl_add_u64 v[56:57], v[224:225], 0, s[88:89]
	s_addc_u32 s23, s23, 0
	s_add_i32 s24, s36, s29
	global_load_lds_dwordx4 v[56:57], off
	v_lshl_add_u64 v[56:57], s[22:23], 0, v[144:145]
	s_mov_b32 m0, s24
	s_nop 0
	global_load_lds_dwordx4 v[56:57], off
	v_lshl_add_u64 v[56:57], s[22:23], 0, v[148:149]
	s_add_i32 m0, s24, 0x2000
	s_nop 0
	global_load_lds_dwordx4 v[56:57], off
	v_lshl_add_u64 v[56:57], v[226:227], 0, s[88:89]
	s_mov_b32 m0, s39
	s_nop 0
	global_load_lds_dwordx4 v[56:57], off
	v_lshl_add_u64 v[56:57], v[228:229], 0, s[88:89]
	s_mov_b32 m0, s40
	s_nop 0
	global_load_lds_dwordx4 v[56:57], off
	s_waitcnt vmcnt(8)
	s_waitcnt lgkmcnt(0)
	s_barrier
	s_waitcnt lgkmcnt(0)
	v_mfma_f32_16x16x32_bf16 v[74:77], v[62:65], v[184:187], v[74:77]
	v_mfma_f32_16x16x32_bf16 v[70:73], v[156:159], v[184:187], v[70:73]
	v_mfma_f32_16x16x32_bf16 v[48:51], v[62:65], v[192:195], v[48:51]
	v_mfma_f32_16x16x32_bf16 v[44:47], v[156:159], v[192:195], v[44:47]
	v_mfma_f32_16x16x32_bf16 v[30:33], v[62:65], v[208:211], v[30:33]
	v_mfma_f32_16x16x32_bf16 v[26:29], v[156:159], v[208:211], v[26:29]
	v_mfma_f32_16x16x32_bf16 v[14:17], v[62:65], v[216:219], v[14:17]
	v_mfma_f32_16x16x32_bf16 v[10:13], v[156:159], v[216:219], v[10:13]
	v_mfma_f32_16x16x32_bf16 v[74:77], v[66:69], v[188:191], v[74:77]
	v_mfma_f32_16x16x32_bf16 v[70:73], v[160:163], v[188:191], v[70:73]
	v_mfma_f32_16x16x32_bf16 v[48:51], v[66:69], v[204:207], v[48:51]
	v_mfma_f32_16x16x32_bf16 v[44:47], v[160:163], v[204:207], v[44:47]
	v_mfma_f32_16x16x32_bf16 v[30:33], v[66:69], v[212:215], v[30:33]
	v_mfma_f32_16x16x32_bf16 v[26:29], v[160:163], v[212:215], v[26:29]
	v_mfma_f32_16x16x32_bf16 v[14:17], v[66:69], v[220:223], v[14:17]
	v_mfma_f32_16x16x32_bf16 v[10:13], v[160:163], v[220:223], v[10:13]
	v_mfma_f32_16x16x32_bf16 v[56:59], v[168:171], v[184:187], v[58:61]
	v_mfma_f32_16x16x32_bf16 v[52:55], v[176:179], v[184:187], v[52:55]
	v_mfma_f32_16x16x32_bf16 v[40:43], v[168:171], v[192:195], v[40:43]
	v_mfma_f32_16x16x32_bf16 v[36:39], v[176:179], v[192:195], v[36:39]
	v_mfma_f32_16x16x32_bf16 v[22:25], v[168:171], v[208:211], v[22:25]
	v_mfma_f32_16x16x32_bf16 v[18:21], v[176:179], v[208:211], v[18:21]
	v_mfma_f32_16x16x32_bf16 v[6:9], v[168:171], v[216:219], v[6:9]
	v_mfma_f32_16x16x32_bf16 v[2:5], v[176:179], v[216:219], v[2:5]
	v_mfma_f32_16x16x32_bf16 v[58:61], v[172:175], v[188:191], v[56:59]
	v_mfma_f32_16x16x32_bf16 v[54:57], v[180:183], v[188:191], v[52:55]
	v_mfma_f32_16x16x32_bf16 v[40:43], v[172:175], v[204:207], v[40:43]
	v_mfma_f32_16x16x32_bf16 v[36:39], v[180:183], v[204:207], v[36:39]
	v_mfma_f32_16x16x32_bf16 v[22:25], v[172:175], v[212:215], v[22:25]
	v_mfma_f32_16x16x32_bf16 v[18:21], v[180:183], v[212:215], v[18:21]
	v_mfma_f32_16x16x32_bf16 v[6:9], v[172:175], v[220:223], v[6:9]
	v_mfma_f32_16x16x32_bf16 v[2:5], v[180:183], v[220:223], v[2:5]
	s_barrier
	s_add_i32 s26, s26, 2
	s_add_u32 s6, s6, 0x100
	s_addc_u32 s7, s7, 0
	s_add_u32 s15, s15, 0x100
	s_addc_u32 s17, s17, 0
	s_cmp_gt_u32 s26, 13
	s_cbranch_scc0 .LBB0_213
	s_and_b64 vcc, exec, s[12:13]
	s_cbranch_vccz .LBB0_216
	s_barrier

; #define PG8_STAGE(bufoff, gbase, voff) do { _Pragma("unroll") for (int _i = 0; _i < 2; ++_i) \
;         __builtin_amdgcn_global_load_lds((const unsigned*)((const char*)(gbase) + (voff)[_i]), (LAS unsigned*)(lds + (bufoff) + ldsw + _i * 8192), 16, 0, 0); } while (0)
; #define PG8_LDA(dst, b, h) do { _Pragma("unroll") for (int m = 0; m < 4; ++m) _Pragma("unroll") for (int k = 0; k < 2; ++k) dst[m][k] = *(const LAS bf16x8*)(lds + PG8_SA(b, h) + aoff + m * 2048 + k * 1024); } while (0)
; #define PG8_LDB(dst, b, h) do { _Pragma("unroll") for (int n = 0; n < 2; ++n) _Pragma("unroll") for (int k = 0; k < 2; ++k) dst[n][k] = *(const LAS bf16x8*)(lds + PG8_SB(b, h) + boff + n * 2048 + k * 1024); } while (0)
; #define PG8_MMA(ai, bj, At, Bt) do { __builtin_amdgcn_s_setprio(1); _Pragma("unroll") for (int m = 0; m < 4; ++m) _Pragma("unroll") for (int n = 0; n < 2; ++n) _Pragma("unroll") for (int k = 0; k < 2; ++k) \
;         acc[ai][bj][m][n] = __builtin_amdgcn_mfma_f32_16x16x32_bf16(Bt[n][k], At[m][k], acc[ai][bj][m][n], 0, 0, 0); __builtin_amdgcn_s_setprio(0); } while (0)
; #define PG8_WAIT_V(n) asm volatile("s_waitcnt vmcnt(" #n ")" ::: "memory")
; #define PG8_WAIT_L(n) asm volatile("s_waitcnt lgkmcnt(" #n ")" ::: "memory")
; #define PG8_BAR __builtin_amdgcn_s_barrier()
; #define PG8_SCHED __builtin_amdgcn_sched_barrier(0)
; #define PG8_WAIT_V(n) asm volatile("s_waitcnt vmcnt(" #n ")" ::: "memory")
; #define PG8_WAIT_L(n) asm volatile("s_waitcnt lgkmcnt(" #n ")" ::: "memory")
;     ...
;         for (int t = 0; t < nt; t += 2) {
;             const bool last = (t == nt - 2);
;             const char* a1 = cA + (size_t)(t + 1) * kstepA;
;             const char* a2 = last ? nA : cA + (size_t)(t + 2) * kstepA; const char* b2 = last ? nB : cB + (size_t)(t + 2) * kstep;
;             const char* a3 = a2 + kstepA; const char* b3 = b2 + kstep;
;             PG8_LDB(B0, 0, 0); PG8_LDB(B1, 0, 1); PG8_SCHED; PG8_LDA(At, 0, 0); PG8_STAGE(PG8_SA(1, 1), a1 + hstepA, voffA);
;             PG8_WAIT_V(8); PG8_WAIT_L(0); PG8_BAR; PG8_MMA(0, 0, At, B0); PG8_MMA(0, 1, At, B1); PG8_BAR; PG8_SCHED;
;             PG8_LDA(At, 0, 1); PG8_STAGE(PG8_SB(0, 0), b2, voffB); PG8_STAGE(PG8_SB(0, 1), b2 + hstep, voffB); PG8_STAGE(PG8_SA(0, 0), a2, voffA);
;             PG8_WAIT_V(8); PG8_WAIT_L(0); PG8_BAR; if (hi_on) { PG8_MMA(1, 0, At, B0); PG8_MMA(1, 1, At, B1); } PG8_BAR; PG8_SCHED;
.LBB0_717:
	s_add_u32 s24, s22, 0x3fc000
	s_addc_u32 s25, s23, 0
	s_cmp_eq_u32 s45, 12
	s_cselect_b32 s28, s18, s24
	s_cselect_b32 s29, s19, s25
	s_cselect_b32 s26, s20, s15
	s_cselect_b32 s27, s21, s17
	s_add_u32 s24, s28, 0x400000
	s_addc_u32 s25, s29, 0
	s_add_i32 s33, 0, 0x10000
	s_add_i32 s48, 0, 0x14000
	v_add_u32_e32 v64, s33, v200
	v_add_u32_e32 v160, s48, v200
	ds_read_b128 v[52:55], v64
	ds_read_b128 v[56:59], v64 offset:1024
	ds_read_b128 v[60:63], v64 offset:2048
	ds_read_b128 v[64:67], v64 offset:3072
	ds_read_b128 v[148:151], v160
	ds_read_b128 v[152:155], v160 offset:1024
	ds_read_b128 v[156:159], v160 offset:2048
	ds_read_b128 v[160:163], v160 offset:3072
	v_lshl_add_u64 v[212:213], s[22:23], 0, v[194:195]
	s_add_i32 m0, s34, 0xc000
	ds_read_b128 v[164:167], v249
	ds_read_b128 v[168:171], v249 offset:1024
	ds_read_b128 v[172:175], v249 offset:2048
	ds_read_b128 v[176:179], v249 offset:3072
	ds_read_b128 v[180:183], v249 offset:4096
	ds_read_b128 v[184:187], v249 offset:5120
	ds_read_b128 v[204:207], v249 offset:6144
	ds_read_b128 v[208:211], v249 offset:7168
	global_load_lds_dwordx4 v[212:213], off
	v_lshl_add_u64 v[212:213], s[22:23], 0, v[196:197]
	s_add_i32 m0, s34, 0xe000
	s_nop 0
	global_load_lds_dwordx4 v[212:213], off
	s_waitcnt vmcnt(8)
	s_waitcnt lgkmcnt(0)
	s_barrier
	s_waitcnt lgkmcnt(0)
	v_mfma_f32_16x16x32_bf16 v[144:147], v[52:55], v[164:167], v[144:147]
	v_mfma_f32_16x16x32_bf16 v[140:143], v[60:63], v[164:167], v[140:143]
	v_mfma_f32_16x16x32_bf16 v[128:131], v[52:55], v[172:175], v[128:131]
	v_mfma_f32_16x16x32_bf16 v[124:127], v[60:63], v[172:175], v[124:127]
	v_mfma_f32_16x16x32_bf16 v[112:115], v[52:55], v[180:183], v[112:115]
	v_mfma_f32_16x16x32_bf16 v[108:111], v[60:63], v[180:183], v[108:111]
	v_mfma_f32_16x16x32_bf16 v[96:99], v[52:55], v[204:207], v[96:99]
	v_mfma_f32_16x16x32_bf16 v[92:95], v[60:63], v[204:207], v[92:95]
	v_mfma_f32_16x16x32_bf16 v[144:147], v[56:59], v[168:171], v[144:147]
	v_mfma_f32_16x16x32_bf16 v[140:143], v[64:67], v[168:171], v[140:143]
	v_mfma_f32_16x16x32_bf16 v[128:131], v[56:59], v[176:179], v[128:131]
	v_mfma_f32_16x16x32_bf16 v[124:127], v[64:67], v[176:179], v[124:127]
	v_mfma_f32_16x16x32_bf16 v[112:115], v[56:59], v[184:187], v[112:115]
	v_mfma_f32_16x16x32_bf16 v[108:111], v[64:67], v[184:187], v[108:111]
	v_mfma_f32_16x16x32_bf16 v[96:99], v[56:59], v[208:211], v[96:99]
	v_mfma_f32_16x16x32_bf16 v[92:95], v[64:67], v[208:211], v[92:95]
	v_mfma_f32_16x16x32_bf16 v[136:139], v[148:151], v[164:167], v[136:139]
	v_mfma_f32_16x16x32_bf16 v[132:135], v[156:159], v[164:167], v[132:135]
	v_mfma_f32_16x16x32_bf16 v[120:123], v[148:151], v[172:175], v[120:123]
	v_mfma_f32_16x16x32_bf16 v[116:119], v[156:159], v[172:175], v[116:119]
	v_mfma_f32_16x16x32_bf16 v[104:107], v[148:151], v[180:183], v[104:107]
	v_mfma_f32_16x16x32_bf16 v[100:103], v[156:159], v[180:183], v[100:103]
	v_mfma_f32_16x16x32_bf16 v[88:91], v[148:151], v[204:207], v[88:91]
	v_mfma_f32_16x16x32_bf16 v[84:87], v[156:159], v[204:207], v[84:87]
	v_mfma_f32_16x16x32_bf16 v[136:139], v[152:155], v[168:171], v[136:139]
	v_mfma_f32_16x16x32_bf16 v[132:135], v[160:163], v[168:171], v[132:135]
	v_mfma_f32_16x16x32_bf16 v[120:123], v[152:155], v[176:179], v[120:123]
	v_mfma_f32_16x16x32_bf16 v[116:119], v[160:163], v[176:179], v[116:119]
	v_mfma_f32_16x16x32_bf16 v[104:107], v[152:155], v[184:187], v[104:107]
	v_mfma_f32_16x16x32_bf16 v[100:103], v[160:163], v[184:187], v[100:103]
	v_mfma_f32_16x16x32_bf16 v[88:91], v[152:155], v[208:211], v[88:91]
	v_mfma_f32_16x16x32_bf16 v[84:87], v[160:163], v[208:211], v[84:87]
	s_barrier
	s_add_i32 s33, s33, s31
	v_lshl_add_u64 v[212:213], s[26:27], 0, v[34:35]
	s_mov_b32 m0, s33
	ds_read_b128 v[164:167], v249 offset:16384
	ds_read_b128 v[168:171], v249 offset:17408
	ds_read_b128 v[172:175], v249 offset:18432
	ds_read_b128 v[176:179], v249 offset:19456
	ds_read_b128 v[180:183], v249 offset:20480
	ds_read_b128 v[184:187], v249 offset:21504
	ds_read_b128 v[204:207], v249 offset:22528
	ds_read_b128 v[208:211], v249 offset:23552
	global_load_lds_dwordx4 v[212:213], off
	s_add_i32 m0, s33, 0x2000
	s_add_u32 s46, s26, 0x40000
	v_lshl_add_u64 v[214:215], s[26:27], 0, v[188:189]
	s_addc_u32 s47, s27, 0
	s_add_i32 s33, s48, s31
	global_load_lds_dwordx4 v[214:215], off
	v_lshl_add_u64 v[216:217], s[46:47], 0, v[34:35]
	s_mov_b32 m0, s33
	s_nop 0
	global_load_lds_dwordx4 v[216:217], off
	v_lshl_add_u64 v[216:217], s[46:47], 0, v[188:189]
	s_add_i32 m0, s33, 0x2000
	s_nop 0
	global_load_lds_dwordx4 v[216:217], off
	v_lshl_add_u64 v[216:217], s[28:29], 0, v[192:193]
	s_mov_b32 m0, s34
	s_nop 0
	global_load_lds_dwordx4 v[216:217], off
	v_lshl_add_u64 v[216:217], s[28:29], 0, v[190:191]
	s_mov_b32 m0, s35
	s_nop 0
	global_load_lds_dwordx4 v[216:217], off
	s_waitcnt vmcnt(8)
	s_waitcnt lgkmcnt(0)
	s_barrier
; #define PG8_STAGE(bufoff, gbase, voff) do { _Pragma("unroll") for (int _i = 0; _i < 2; ++_i) \
;         __builtin_amdgcn_global_load_lds((const unsigned*)((const char*)(gbase) + (voff)[_i]), (LAS unsigned*)(lds + (bufoff) + ldsw + _i * 8192), 16, 0, 0); } while (0)
; #define PG8_LDA(dst, b, h) do { _Pragma("unroll") for (int m = 0; m < 4; ++m) _Pragma("unroll") for (int k = 0; k < 2; ++k) dst[m][k] = *(const LAS bf16x8*)(lds + PG8_SA(b, h) + aoff + m * 2048 + k * 1024); } while (0)
; #define PG8_LDB(dst, b, h) do { _Pragma("unroll") for (int n = 0; n < 2; ++n) _Pragma("unroll") for (int k = 0; k < 2; ++k) dst[n][k] = *(const LAS bf16x8*)(lds + PG8_SB(b, h) + boff + n * 2048 + k * 1024); } while (0)
; #define PG8_MMA(ai, bj, At, Bt) do { __builtin_amdgcn_s_setprio(1); _Pragma("unroll") for (int m = 0; m < 4; ++m) _Pragma("unroll") for (int n = 0; n < 2; ++n) _Pragma("unroll") for (int k = 0; k < 2; ++k) \
;         acc[ai][bj][m][n] = __builtin_amdgcn_mfma_f32_16x16x32_bf16(Bt[n][k], At[m][k], acc[ai][bj][m][n], 0, 0, 0); __builtin_amdgcn_s_setprio(0); } while (0)
; #define PG8_WAIT_V(n) asm volatile("s_waitcnt vmcnt(" #n ")" ::: "memory")
; #define PG8_WAIT_L(n) asm volatile("s_waitcnt lgkmcnt(" #n ")" ::: "memory")
; #define PG8_BAR __builtin_amdgcn_s_barrier()
; #define PG8_SCHED __builtin_amdgcn_sched_barrier(0)
; #define PG8_STAGE(bufoff, gbase, voff) do { _Pragma("unroll") for (int _i = 0; _i < 2; ++_i) \
;         __builtin_amdgcn_global_load_lds((const unsigned*)((const char*)(gbase) + (voff)[_i]), (LAS unsigned*)(lds + (bufoff) + ldsw + _i * 8192), 16, 0, 0); } while (0)
; #define PG8_LDA(dst, b, h) do { _Pragma("unroll") for (int m = 0; m < 4; ++m) _Pragma("unroll") for (int k = 0; k < 2; ++k) dst[m][k] = *(const LAS bf16x8*)(lds + PG8_SA(b, h) + aoff + m * 2048 + k * 1024); } while (0)
; #define PG8_WAIT_V(n) asm volatile("s_waitcnt vmcnt(" #n ")" ::: "memory")
; #define PG8_WAIT_L(n) asm volatile("s_waitcnt lgkmcnt(" #n ")" ::: "memory")
;     ...
;             PG8_WAIT_V(8); PG8_WAIT_L(0); PG8_BAR; if (hi_on) { PG8_MMA(1, 0, At, B0); PG8_MMA(1, 1, At, B1); } PG8_BAR; PG8_SCHED;
;             PG8_LDB(B0, 1, 0); PG8_LDB(B1, 1, 1); PG8_SCHED; PG8_LDA(At, 1, 0); PG8_STAGE(PG8_SA(0, 1), a2 + hstepA, voffA);
;             PG8_WAIT_V(8); PG8_WAIT_L(0); PG8_BAR; PG8_MMA(0, 0, At, B0); PG8_MMA(0, 1, At, B1); PG8_BAR; PG8_SCHED;
	s_waitcnt lgkmcnt(0)
	v_mfma_f32_16x16x32_bf16 v[80:83], v[52:55], v[164:167], v[80:83]
	v_mfma_f32_16x16x32_bf16 v[76:79], v[60:63], v[164:167], v[76:79]
	v_mfma_f32_16x16x32_bf16 v[48:51], v[52:55], v[172:175], v[48:51]
	v_mfma_f32_16x16x32_bf16 v[44:47], v[60:63], v[172:175], v[44:47]
	v_mfma_f32_16x16x32_bf16 v[30:33], v[52:55], v[180:183], v[30:33]
	v_mfma_f32_16x16x32_bf16 v[26:29], v[60:63], v[180:183], v[26:29]
	v_mfma_f32_16x16x32_bf16 v[14:17], v[52:55], v[204:207], v[14:17]
	v_mfma_f32_16x16x32_bf16 v[10:13], v[60:63], v[204:207], v[10:13]
	v_mfma_f32_16x16x32_bf16 v[80:83], v[56:59], v[168:171], v[80:83]
	v_mfma_f32_16x16x32_bf16 v[76:79], v[64:67], v[168:171], v[76:79]
	v_mfma_f32_16x16x32_bf16 v[48:51], v[56:59], v[176:179], v[48:51]
	v_mfma_f32_16x16x32_bf16 v[44:47], v[64:67], v[176:179], v[44:47]
	v_mfma_f32_16x16x32_bf16 v[30:33], v[56:59], v[184:187], v[30:33]
	v_mfma_f32_16x16x32_bf16 v[26:29], v[64:67], v[184:187], v[26:29]
	v_mfma_f32_16x16x32_bf16 v[14:17], v[56:59], v[208:211], v[14:17]
	v_mfma_f32_16x16x32_bf16 v[10:13], v[64:67], v[208:211], v[10:13]
	v_mfma_f32_16x16x32_bf16 v[40:43], v[148:151], v[172:175], v[40:43]
	v_mfma_f32_16x16x32_bf16 v[36:39], v[156:159], v[172:175], v[36:39]
	v_mfma_f32_16x16x32_bf16 v[22:25], v[148:151], v[180:183], v[22:25]
	v_mfma_f32_16x16x32_bf16 v[18:21], v[156:159], v[180:183], v[18:21]
	v_mfma_f32_16x16x32_bf16 v[6:9], v[148:151], v[204:207], v[6:9]
	v_mfma_f32_16x16x32_bf16 v[2:5], v[156:159], v[204:207], v[2:5]
	v_mfma_f32_16x16x32_bf16 v[52:55], v[148:151], v[164:167], v[72:75]
	v_mfma_f32_16x16x32_bf16 v[56:59], v[156:159], v[164:167], v[68:71]
	v_mfma_f32_16x16x32_bf16 v[40:43], v[152:155], v[176:179], v[40:43]
	v_mfma_f32_16x16x32_bf16 v[36:39], v[160:163], v[176:179], v[36:39]
	v_mfma_f32_16x16x32_bf16 v[22:25], v[152:155], v[184:187], v[22:25]
	v_mfma_f32_16x16x32_bf16 v[18:21], v[160:163], v[184:187], v[18:21]
	v_mfma_f32_16x16x32_bf16 v[6:9], v[152:155], v[208:211], v[6:9]
	v_mfma_f32_16x16x32_bf16 v[2:5], v[160:163], v[208:211], v[2:5]
	v_mfma_f32_16x16x32_bf16 v[52:55], v[152:155], v[168:171], v[52:55]
	v_mfma_f32_16x16x32_bf16 v[56:59], v[160:163], v[168:171], v[56:59]
	s_barrier
	s_add_i32 s33, 0, 0x18000
	s_add_i32 s46, 0, 0x1c000
	v_add_u32_e32 v72, s33, v200
	v_add_u32_e32 v160, s46, v200
	ds_read_b128 v[60:63], v72
	ds_read_b128 v[64:67], v72 offset:1024
	ds_read_b128 v[68:71], v72 offset:2048
	ds_read_b128 v[72:75], v72 offset:3072
	ds_read_b128 v[148:151], v160
	ds_read_b128 v[152:155], v160 offset:1024
	ds_read_b128 v[156:159], v160 offset:2048
	ds_read_b128 v[160:163], v160 offset:3072
	s_add_u32 s28, s28, 0x4000
	s_addc_u32 s29, s29, 0
	s_mov_b32 m0, s38
	v_lshl_add_u64 v[216:217], s[28:29], 0, v[192:193]
	ds_read_b128 v[164:167], v249 offset:32768
	ds_read_b128 v[168:171], v249 offset:33792
	ds_read_b128 v[172:175], v249 offset:34816
	ds_read_b128 v[176:179], v249 offset:35840
	ds_read_b128 v[180:183], v249 offset:36864
	ds_read_b128 v[184:187], v249 offset:37888
	ds_read_b128 v[204:207], v249 offset:38912
	ds_read_b128 v[208:211], v249 offset:39936
	global_load_lds_dwordx4 v[216:217], off
	v_lshl_add_u64 v[216:217], s[28:29], 0, v[190:191]
	s_mov_b32 m0, s39
	s_nop 0
	global_load_lds_dwordx4 v[216:217], off
	s_waitcnt vmcnt(8)
	s_waitcnt lgkmcnt(0)
	s_barrier
	s_waitcnt lgkmcnt(0)
	v_mfma_f32_16x16x32_bf16 v[144:147], v[60:63], v[164:167], v[144:147]
	v_mfma_f32_16x16x32_bf16 v[140:143], v[68:71], v[164:167], v[140:143]
	v_mfma_f32_16x16x32_bf16 v[128:131], v[60:63], v[172:175], v[128:131]
	v_mfma_f32_16x16x32_bf16 v[124:127], v[68:71], v[172:175], v[124:127]
	v_mfma_f32_16x16x32_bf16 v[112:115], v[60:63], v[180:183], v[112:115]
	v_mfma_f32_16x16x32_bf16 v[108:111], v[68:71], v[180:183], v[108:111]
	v_mfma_f32_16x16x32_bf16 v[96:99], v[60:63], v[204:207], v[96:99]
	v_mfma_f32_16x16x32_bf16 v[92:95], v[68:71], v[204:207], v[92:95]
	v_mfma_f32_16x16x32_bf16 v[144:147], v[64:67], v[168:171], v[144:147]
	v_mfma_f32_16x16x32_bf16 v[140:143], v[72:75], v[168:171], v[140:143]
	v_mfma_f32_16x16x32_bf16 v[128:131], v[64:67], v[176:179], v[128:131]
	v_mfma_f32_16x16x32_bf16 v[124:127], v[72:75], v[176:179], v[124:127]
	v_mfma_f32_16x16x32_bf16 v[112:115], v[64:67], v[184:187], v[112:115]
	v_mfma_f32_16x16x32_bf16 v[108:111], v[72:75], v[184:187], v[108:111]
	v_mfma_f32_16x16x32_bf16 v[96:99], v[64:67], v[208:211], v[96:99]
	v_mfma_f32_16x16x32_bf16 v[92:95], v[72:75], v[208:211], v[92:95]
	v_mfma_f32_16x16x32_bf16 v[136:139], v[148:151], v[164:167], v[136:139]
	v_mfma_f32_16x16x32_bf16 v[132:135], v[156:159], v[164:167], v[132:135]
	v_mfma_f32_16x16x32_bf16 v[120:123], v[148:151], v[172:175], v[120:123]
	v_mfma_f32_16x16x32_bf16 v[116:119], v[156:159], v[172:175], v[116:119]
	v_mfma_f32_16x16x32_bf16 v[104:107], v[148:151], v[180:183], v[104:107]
	v_mfma_f32_16x16x32_bf16 v[100:103], v[156:159], v[180:183], v[100:103]
	v_mfma_f32_16x16x32_bf16 v[88:91], v[148:151], v[204:207], v[88:91]
	v_mfma_f32_16x16x32_bf16 v[84:87], v[156:159], v[204:207], v[84:87]
	v_mfma_f32_16x16x32_bf16 v[136:139], v[152:155], v[168:171], v[136:139]
	v_mfma_f32_16x16x32_bf16 v[132:135], v[160:163], v[168:171], v[132:135]
	v_mfma_f32_16x16x32_bf16 v[120:123], v[152:155], v[176:179], v[120:123]
	v_mfma_f32_16x16x32_bf16 v[116:119], v[160:163], v[176:179], v[116:119]
	v_mfma_f32_16x16x32_bf16 v[104:107], v[152:155], v[184:187], v[104:107]
	v_mfma_f32_16x16x32_bf16 v[100:103], v[160:163], v[184:187], v[100:103]
	v_mfma_f32_16x16x32_bf16 v[88:91], v[152:155], v[208:211], v[88:91]
	v_mfma_f32_16x16x32_bf16 v[84:87], v[160:163], v[208:211], v[84:87]
	s_barrier
; #define PG8_STAGE(bufoff, gbase, voff) do { _Pragma("unroll") for (int _i = 0; _i < 2; ++_i) \
;         __builtin_amdgcn_global_load_lds((const unsigned*)((const char*)(gbase) + (voff)[_i]), (LAS unsigned*)(lds + (bufoff) + ldsw + _i * 8192), 16, 0, 0); } while (0)
; #define PG8_LDA(dst, b, h) do { _Pragma("unroll") for (int m = 0; m < 4; ++m) _Pragma("unroll") for (int k = 0; k < 2; ++k) dst[m][k] = *(const LAS bf16x8*)(lds + PG8_SA(b, h) + aoff + m * 2048 + k * 1024); } while (0)
; #define PG8_MMA(ai, bj, At, Bt) do { __builtin_amdgcn_s_setprio(1); _Pragma("unroll") for (int m = 0; m < 4; ++m) _Pragma("unroll") for (int n = 0; n < 2; ++n) _Pragma("unroll") for (int k = 0; k < 2; ++k) \
;         acc[ai][bj][m][n] = __builtin_amdgcn_mfma_f32_16x16x32_bf16(Bt[n][k], At[m][k], acc[ai][bj][m][n], 0, 0, 0); __builtin_amdgcn_s_setprio(0); } while (0)
; #define PG8_WAIT_V(n) asm volatile("s_waitcnt vmcnt(" #n ")" ::: "memory")
; #define PG8_WAIT_L(n) asm volatile("s_waitcnt lgkmcnt(" #n ")" ::: "memory")
; #define PG8_BAR __builtin_amdgcn_s_barrier()
; #define PG8_SCHED __builtin_amdgcn_sched_barrier(0)
; #define PG8_STAGE(bufoff, gbase, voff) do { _Pragma("unroll") for (int _i = 0; _i < 2; ++_i) \
;         __builtin_amdgcn_global_load_lds((const unsigned*)((const char*)(gbase) + (voff)[_i]), (LAS unsigned*)(lds + (bufoff) + ldsw + _i * 8192), 16, 0, 0); } while (0)
; #define PG8_LDA(dst, b, h) do { _Pragma("unroll") for (int m = 0; m < 4; ++m) _Pragma("unroll") for (int k = 0; k < 2; ++k) dst[m][k] = *(const LAS bf16x8*)(lds + PG8_SA(b, h) + aoff + m * 2048 + k * 1024); } while (0)
; #define PG8_MMA(ai, bj, At, Bt) do { __builtin_amdgcn_s_setprio(1); _Pragma("unroll") for (int m = 0; m < 4; ++m) _Pragma("unroll") for (int n = 0; n < 2; ++n) _Pragma("unroll") for (int k = 0; k < 2; ++k) \
;         acc[ai][bj][m][n] = __builtin_amdgcn_mfma_f32_16x16x32_bf16(Bt[n][k], At[m][k], acc[ai][bj][m][n], 0, 0, 0); __builtin_amdgcn_s_setprio(0); } while (0)
; #define PG8_WAIT_V(n) asm volatile("s_waitcnt vmcnt(" #n ")" ::: "memory")
;     ...
;             PG8_LDA(At, 1, 1); PG8_STAGE(PG8_SB(1, 0), b3, voffB); PG8_STAGE(PG8_SB(1, 1), b3 + hstep, voffB); PG8_STAGE(PG8_SA(1, 0), a3, voffA);
;             PG8_WAIT_V(8); PG8_WAIT_L(0); PG8_BAR; if (hi_on) { PG8_MMA(1, 0, At, B0); PG8_MMA(1, 1, At, B1); } PG8_BAR; PG8_SCHED;
;         }
;         if (wr == 0) PG8_BAR;
	s_add_i32 s28, s33, s31
	v_lshl_add_u64 v[212:213], v[212:213], 0, s[88:89]
	s_mov_b32 m0, s28
	ds_read_b128 v[164:167], v249 offset:49152
	ds_read_b128 v[168:171], v249 offset:50176
	ds_read_b128 v[172:175], v249 offset:51200
	ds_read_b128 v[176:179], v249 offset:52224
	ds_read_b128 v[180:183], v249 offset:53248
	ds_read_b128 v[184:187], v249 offset:54272
	ds_read_b128 v[204:207], v249 offset:55296
	ds_read_b128 v[208:211], v249 offset:56320
	global_load_lds_dwordx4 v[212:213], off
	s_add_i32 m0, s28, 0x2000
	s_add_u32 s26, s26, 0x40080
	v_lshl_add_u64 v[212:213], v[214:215], 0, s[88:89]
	s_addc_u32 s27, s27, 0
	s_add_i32 s28, s46, s31
	global_load_lds_dwordx4 v[212:213], off
	v_lshl_add_u64 v[212:213], s[26:27], 0, v[34:35]
	s_mov_b32 m0, s28
	s_nop 0
	global_load_lds_dwordx4 v[212:213], off
	v_lshl_add_u64 v[212:213], s[26:27], 0, v[188:189]
	s_add_i32 m0, s28, 0x2000
	s_nop 0
	global_load_lds_dwordx4 v[212:213], off
	v_lshl_add_u64 v[212:213], s[24:25], 0, v[192:193]
	s_mov_b32 m0, s41
	s_nop 0
	global_load_lds_dwordx4 v[212:213], off
	v_lshl_add_u64 v[212:213], s[24:25], 0, v[190:191]
	s_mov_b32 m0, s42
	s_nop 0
	global_load_lds_dwordx4 v[212:213], off
	s_waitcnt vmcnt(8)
	s_waitcnt lgkmcnt(0)
	s_barrier
	s_waitcnt lgkmcnt(0)
	v_mfma_f32_16x16x32_bf16 v[80:83], v[60:63], v[164:167], v[80:83]
	v_mfma_f32_16x16x32_bf16 v[76:79], v[68:71], v[164:167], v[76:79]
	v_mfma_f32_16x16x32_bf16 v[48:51], v[60:63], v[172:175], v[48:51]
	v_mfma_f32_16x16x32_bf16 v[44:47], v[68:71], v[172:175], v[44:47]
	v_mfma_f32_16x16x32_bf16 v[30:33], v[60:63], v[180:183], v[30:33]
	v_mfma_f32_16x16x32_bf16 v[26:29], v[68:71], v[180:183], v[26:29]
	v_mfma_f32_16x16x32_bf16 v[14:17], v[60:63], v[204:207], v[14:17]
	v_mfma_f32_16x16x32_bf16 v[10:13], v[68:71], v[204:207], v[10:13]
	v_mfma_f32_16x16x32_bf16 v[80:83], v[64:67], v[168:171], v[80:83]
	v_mfma_f32_16x16x32_bf16 v[76:79], v[72:75], v[168:171], v[76:79]
	v_mfma_f32_16x16x32_bf16 v[48:51], v[64:67], v[176:179], v[48:51]
	v_mfma_f32_16x16x32_bf16 v[44:47], v[72:75], v[176:179], v[44:47]
	v_mfma_f32_16x16x32_bf16 v[30:33], v[64:67], v[184:187], v[30:33]
	v_mfma_f32_16x16x32_bf16 v[26:29], v[72:75], v[184:187], v[26:29]
	v_mfma_f32_16x16x32_bf16 v[14:17], v[64:67], v[208:211], v[14:17]
	v_mfma_f32_16x16x32_bf16 v[10:13], v[72:75], v[208:211], v[10:13]
	v_mfma_f32_16x16x32_bf16 v[52:55], v[148:151], v[164:167], v[52:55]
	v_mfma_f32_16x16x32_bf16 v[72:75], v[152:155], v[168:171], v[52:55]
	v_mfma_f32_16x16x32_bf16 v[52:55], v[156:159], v[164:167], v[56:59]
	v_mfma_f32_16x16x32_bf16 v[40:43], v[148:151], v[172:175], v[40:43]
	v_mfma_f32_16x16x32_bf16 v[36:39], v[156:159], v[172:175], v[36:39]
	v_mfma_f32_16x16x32_bf16 v[22:25], v[148:151], v[180:183], v[22:25]
	v_mfma_f32_16x16x32_bf16 v[18:21], v[156:159], v[180:183], v[18:21]
	v_mfma_f32_16x16x32_bf16 v[6:9], v[148:151], v[204:207], v[6:9]
	v_mfma_f32_16x16x32_bf16 v[2:5], v[156:159], v[204:207], v[2:5]
	v_mfma_f32_16x16x32_bf16 v[68:71], v[160:163], v[168:171], v[52:55]
	v_mfma_f32_16x16x32_bf16 v[40:43], v[152:155], v[176:179], v[40:43]
	v_mfma_f32_16x16x32_bf16 v[36:39], v[160:163], v[176:179], v[36:39]
	v_mfma_f32_16x16x32_bf16 v[22:25], v[152:155], v[184:187], v[22:25]
	v_mfma_f32_16x16x32_bf16 v[18:21], v[160:163], v[184:187], v[18:21]
	v_mfma_f32_16x16x32_bf16 v[6:9], v[152:155], v[208:211], v[6:9]
	v_mfma_f32_16x16x32_bf16 v[2:5], v[160:163], v[208:211], v[2:5]
	s_barrier
	s_add_i32 s45, s45, 2
	s_add_u32 s15, s15, 0x100
	s_addc_u32 s17, s17, 0
	s_add_u32 s22, s22, 0x800000
	s_addc_u32 s23, s23, 0
	s_cmp_gt_u32 s45, 13
	s_cbranch_scc0 .LBB0_717
	s_and_b64 vcc, exec, s[10:11]
	s_cbranch_vccz .LBB0_720
	s_barrier

; #define PG8_STAGE(bufoff, gbase, voff) do { _Pragma("unroll") for (int _i = 0; _i < 2; ++_i) \
;         __builtin_amdgcn_global_load_lds((const unsigned*)((const char*)(gbase) + (voff)[_i]), (LAS unsigned*)(lds + (bufoff) + ldsw + _i * 8192), 16, 0, 0); } while (0)
; #define PG8_LDA(dst, b, h) do { _Pragma("unroll") for (int m = 0; m < 4; ++m) _Pragma("unroll") for (int k = 0; k < 2; ++k) dst[m][k] = *(const LAS bf16x8*)(lds + PG8_SA(b, h) + aoff + m * 2048 + k * 1024); } while (0)
; #define PG8_LDB(dst, b, h) do { _Pragma("unroll") for (int n = 0; n < 2; ++n) _Pragma("unroll") for (int k = 0; k < 2; ++k) dst[n][k] = *(const LAS bf16x8*)(lds + PG8_SB(b, h) + boff + n * 2048 + k * 1024); } while (0)
; #define PG8_MMA(ai, bj, At, Bt) do { __builtin_amdgcn_s_setprio(1); _Pragma("unroll") for (int m = 0; m < 4; ++m) _Pragma("unroll") for (int n = 0; n < 2; ++n) _Pragma("unroll") for (int k = 0; k < 2; ++k) \
;         acc[ai][bj][m][n] = __builtin_amdgcn_mfma_f32_16x16x32_bf16(Bt[n][k], At[m][k], acc[ai][bj][m][n], 0, 0, 0); __builtin_amdgcn_s_setprio(0); } while (0)
; #define PG8_BAR __builtin_amdgcn_s_barrier()
; template <class Epi, class Sched>
; __device__ __forceinline__ void gemm_phase_gather(LAS unsigned char* lds, const int K, const Sched& S, const Epi& E, const char* Ag, const int* list, const LAS int* seg) {
;     ...
;         for (int t = 0; t < nt; t += 2) {
;             const bool last = (t == nt - 2);
;             const char* a1 = cA + (size_t)(t + 1) * kstep;
;             const char* a2 = last ? cA : cA + (size_t)(t + 2) * kstep; const char* b2 = last ? nB : cB + (size_t)(t + 2) * kstep;
;             unsigned x0[2], x1[2];
;             x0[0] = last ? na0[0] : ca0[0]; x0[1] = last ? na0[1] : ca0[1]; x1[0] = last ? na1[0] : ca1[0]; x1[1] = last ? na1[1] : ca1[1];
;             const char* a3 = a2 + kstep; const char* b3 = b2 + kstep;
;             PG8_LDB(B0, 0, 0); PG8_LDB(B1, 0, 1); PG8_SCHED; PG8_LDA(At, 0, 0); PG8_STAGE(PG8_SA(1, 1), a1, ca1);
;             PG8_WAIT_V(8); PG8_WAIT_L(0); PG8_BAR; PG8_MMA(0, 0, At, B0); PG8_MMA(0, 1, At, B1); PG8_BAR; PG8_SCHED;
;             PG8_LDA(At, 0, 1); PG8_STAGE(PG8_SB(0, 0), b2, voffB); PG8_STAGE(PG8_SB(0, 1), b2 + hstep, voffB); PG8_STAGE(PG8_SA(0, 0), a2, x0);
;             PG8_WAIT_V(8); PG8_WAIT_L(0); PG8_BAR; if (hi_on) { PG8_MMA(1, 0, At, B0); PG8_MMA(1, 1, At, B1); } PG8_BAR; PG8_SCHED;
.LBB0_1035:
	s_add_u32 s6, s92, s36
	s_addc_u32 s7, s93, s37
	s_add_u32 s33, s6, 0x7c00100
	s_addc_u32 s38, s7, 0
	s_add_u32 s58, s54, s36
	s_addc_u32 s39, s55, s37
	s_add_i32 s59, 0, 0x10000
	s_cmpk_eq_i32 s36, 0x700
	s_cselect_b64 s[6:7], -1, 0
	s_and_b64 s[8:9], s[6:7], exec
	s_cselect_b32 s41, s81, s38
	s_cselect_b32 s40, s80, s33
	s_cselect_b32 s39, s75, s39
	s_cselect_b32 s38, s78, s58
	s_add_i32 s33, 0, 0x14000
	v_add_u32_e32 v134, s59, v248
	v_add_u32_e32 v146, s33, v248
	ds_read_b128 v[150:153], v134
	ds_read_b128 v[154:157], v134 offset:1024
	ds_read_b128 v[158:161], v134 offset:2048
	ds_read_b128 v[162:165], v134 offset:3072
	ds_read_b128 v[134:137], v146
	ds_read_b128 v[138:141], v146 offset:1024
	ds_read_b128 v[142:145], v146 offset:2048
	ds_read_b128 v[146:149], v146 offset:3072
	v_cndmask_b32_e64 v34, v209, v228, s[6:7]
	v_cndmask_b32_e64 v222, v212, v246, s[6:7]
	v_lshl_add_u64 v[218:219], v[216:217], 0, s[36:37]
	s_add_i32 m0, s15, 0xc000
	s_waitcnt lgkmcnt(0)
	ds_read_b128 v[166:169], v213
	ds_read_b128 v[170:173], v213 offset:1024
	ds_read_b128 v[174:177], v213 offset:2048
	ds_read_b128 v[178:181], v213 offset:3072
	ds_read_b128 v[182:185], v213 offset:4096
	ds_read_b128 v[186:189], v213 offset:5120
	ds_read_b128 v[190:193], v213 offset:6144
	ds_read_b128 v[194:197], v213 offset:7168
	global_load_lds_dwordx4 v[218:219], off
	v_lshl_add_u64 v[218:219], v[36:37], 0, s[36:37]
	s_add_i32 m0, s15, 0xe000
	s_nop 0
	global_load_lds_dwordx4 v[218:219], off
	s_waitcnt vmcnt(8)
	s_waitcnt lgkmcnt(0)
	s_barrier
	s_waitcnt lgkmcnt(0)
	v_mfma_f32_16x16x32_bf16 v[74:77], v[150:153], v[166:169], v[74:77]
	v_mfma_f32_16x16x32_bf16 v[130:133], v[158:161], v[166:169], v[130:133]
	v_mfma_f32_16x16x32_bf16 v[126:129], v[150:153], v[174:177], v[126:129]
	v_mfma_f32_16x16x32_bf16 v[122:125], v[158:161], v[174:177], v[122:125]
	v_mfma_f32_16x16x32_bf16 v[118:121], v[150:153], v[182:185], v[118:121]
	v_mfma_f32_16x16x32_bf16 v[114:117], v[158:161], v[182:185], v[114:117]
	v_mfma_f32_16x16x32_bf16 v[110:113], v[150:153], v[190:193], v[110:113]
	v_mfma_f32_16x16x32_bf16 v[106:109], v[158:161], v[190:193], v[106:109]
	v_mfma_f32_16x16x32_bf16 v[74:77], v[154:157], v[170:173], v[74:77]
	v_mfma_f32_16x16x32_bf16 v[130:133], v[162:165], v[170:173], v[130:133]
	v_mfma_f32_16x16x32_bf16 v[126:129], v[154:157], v[178:181], v[126:129]
	v_mfma_f32_16x16x32_bf16 v[122:125], v[162:165], v[178:181], v[122:125]
	v_mfma_f32_16x16x32_bf16 v[118:121], v[154:157], v[186:189], v[118:121]
	v_mfma_f32_16x16x32_bf16 v[114:117], v[162:165], v[186:189], v[114:117]
	v_mfma_f32_16x16x32_bf16 v[110:113], v[154:157], v[194:197], v[110:113]
	v_mfma_f32_16x16x32_bf16 v[106:109], v[162:165], v[194:197], v[106:109]
	v_mfma_f32_16x16x32_bf16 v[102:105], v[134:137], v[166:169], v[102:105]
	v_mfma_f32_16x16x32_bf16 v[98:101], v[142:145], v[166:169], v[98:101]
	v_mfma_f32_16x16x32_bf16 v[94:97], v[134:137], v[174:177], v[94:97]
	v_mfma_f32_16x16x32_bf16 v[90:93], v[142:145], v[174:177], v[90:93]
	v_mfma_f32_16x16x32_bf16 v[86:89], v[134:137], v[182:185], v[86:89]
	v_mfma_f32_16x16x32_bf16 v[82:85], v[142:145], v[182:185], v[82:85]
	v_mfma_f32_16x16x32_bf16 v[78:81], v[134:137], v[190:193], v[78:81]
	v_mfma_f32_16x16x32_bf16 v[70:73], v[142:145], v[190:193], v[70:73]
	v_mfma_f32_16x16x32_bf16 v[102:105], v[138:141], v[170:173], v[102:105]
	v_mfma_f32_16x16x32_bf16 v[98:101], v[146:149], v[170:173], v[98:101]
	v_mfma_f32_16x16x32_bf16 v[94:97], v[138:141], v[178:181], v[94:97]
	v_mfma_f32_16x16x32_bf16 v[90:93], v[146:149], v[178:181], v[90:93]
	v_mfma_f32_16x16x32_bf16 v[86:89], v[138:141], v[186:189], v[86:89]
	v_mfma_f32_16x16x32_bf16 v[82:85], v[146:149], v[186:189], v[82:85]
	v_mfma_f32_16x16x32_bf16 v[78:81], v[138:141], v[194:197], v[78:81]
	v_mfma_f32_16x16x32_bf16 v[70:73], v[146:149], v[194:197], v[70:73]
	s_barrier
	s_add_i32 s8, s59, s13
	v_lshl_add_u64 v[218:219], s[38:39], 0, v[204:205]
	s_mov_b32 m0, s8
	ds_read_b128 v[190:193], v213 offset:16384
	ds_read_b128 v[194:197], v213 offset:17408
	ds_read_b128 v[182:185], v213 offset:18432
	ds_read_b128 v[186:189], v213 offset:19456
	ds_read_b128 v[174:177], v213 offset:20480
	ds_read_b128 v[178:181], v213 offset:21504
	ds_read_b128 v[166:169], v213 offset:22528
	ds_read_b128 v[170:173], v213 offset:23552
	global_load_lds_dwordx4 v[218:219], off
	s_add_i32 m0, s8, 0x2000
	s_add_u32 s8, s38, 0x40000
	v_lshl_add_u64 v[220:221], s[38:39], 0, v[206:207]
	s_addc_u32 s9, s39, 0
	s_add_i32 s33, s33, s13
	global_load_lds_dwordx4 v[220:221], off
	v_lshl_add_u64 v[230:231], s[8:9], 0, v[204:205]
	s_mov_b32 m0, s33
	v_cndmask_b32_e64 v211, 0, 1, s[4:5]
	global_load_lds_dwordx4 v[230:231], off
	v_lshl_add_u64 v[230:231], s[8:9], 0, v[206:207]
	s_add_i32 m0, s33, 0x2000
	v_cmp_ne_u32_e64 s[8:9], 1, v211
	global_load_lds_dwordx4 v[230:231], off
	s_mov_b32 m0, s15
	s_andn2_b64 vcc, exec, s[4:5]
	global_load_lds_dwordx4 v34, s[40:41]
	s_mov_b32 m0, s17
	s_nop 0
	global_load_lds_dwordx4 v222, s[40:41]
	s_waitcnt vmcnt(8)
	s_waitcnt lgkmcnt(0)
	s_barrier
	s_cbranch_vccnz .LBB0_1037
; #define PG8_MMA(ai, bj, At, Bt) do { __builtin_amdgcn_s_setprio(1); _Pragma("unroll") for (int m = 0; m < 4; ++m) _Pragma("unroll") for (int n = 0; n < 2; ++n) _Pragma("unroll") for (int k = 0; k < 2; ++k) \
;         acc[ai][bj][m][n] = __builtin_amdgcn_mfma_f32_16x16x32_bf16(Bt[n][k], At[m][k], acc[ai][bj][m][n], 0, 0, 0); __builtin_amdgcn_s_setprio(0); } while (0)
; #define PG8_WAIT_V(n) asm volatile("s_waitcnt vmcnt(" #n ")" ::: "memory")
; #define PG8_WAIT_L(n) asm volatile("s_waitcnt lgkmcnt(" #n ")" ::: "memory")
; #define PG8_BAR __builtin_amdgcn_s_barrier()
; #define PG8_SCHED __builtin_amdgcn_sched_barrier(0)
; #define PG8_MMA(ai, bj, At, Bt) do { __builtin_amdgcn_s_setprio(1); _Pragma("unroll") for (int m = 0; m < 4; ++m) _Pragma("unroll") for (int n = 0; n < 2; ++n) _Pragma("unroll") for (int k = 0; k < 2; ++k) \
;         acc[ai][bj][m][n] = __builtin_amdgcn_mfma_f32_16x16x32_bf16(Bt[n][k], At[m][k], acc[ai][bj][m][n], 0, 0, 0); __builtin_amdgcn_s_setprio(0); } while (0)
; #define PG8_WAIT_V(n) asm volatile("s_waitcnt vmcnt(" #n ")" ::: "memory")
; #define PG8_WAIT_L(n) asm volatile("s_waitcnt lgkmcnt(" #n ")" ::: "memory")
; #define PG8_BAR __builtin_amdgcn_s_barrier()
; #define PG8_SCHED __builtin_amdgcn_sched_barrier(0)
; template <class Epi, class Sched>
; __device__ __forceinline__ void gemm_phase_gather(LAS unsigned char* lds, const int K, const Sched& S, const Epi& E, const char* Ag, const int* list, const LAS int* seg) {
;     ...
;             PG8_WAIT_V(8); PG8_WAIT_L(0); PG8_BAR; if (hi_on) { PG8_MMA(1, 0, At, B0); PG8_MMA(1, 1, At, B1); } PG8_BAR; PG8_SCHED;
	s_waitcnt lgkmcnt(0)
	v_mfma_f32_16x16x32_bf16 v[66:69], v[150:153], v[190:193], v[66:69]
	v_mfma_f32_16x16x32_bf16 v[62:65], v[158:161], v[190:193], v[62:65]
	v_mfma_f32_16x16x32_bf16 v[58:61], v[150:153], v[182:185], v[58:61]
	v_mfma_f32_16x16x32_bf16 v[54:57], v[158:161], v[182:185], v[54:57]
	v_mfma_f32_16x16x32_bf16 v[50:53], v[150:153], v[174:177], v[50:53]
	v_mfma_f32_16x16x32_bf16 v[46:49], v[158:161], v[174:177], v[46:49]
	v_mfma_f32_16x16x32_bf16 v[42:45], v[150:153], v[166:169], v[42:45]
	v_mfma_f32_16x16x32_bf16 v[38:41], v[158:161], v[166:169], v[38:41]
	v_mfma_f32_16x16x32_bf16 v[66:69], v[154:157], v[194:197], v[66:69]
	v_mfma_f32_16x16x32_bf16 v[62:65], v[162:165], v[194:197], v[62:65]
	v_mfma_f32_16x16x32_bf16 v[58:61], v[154:157], v[186:189], v[58:61]
	v_mfma_f32_16x16x32_bf16 v[54:57], v[162:165], v[186:189], v[54:57]
	v_mfma_f32_16x16x32_bf16 v[50:53], v[154:157], v[178:181], v[50:53]
	v_mfma_f32_16x16x32_bf16 v[46:49], v[162:165], v[178:181], v[46:49]
	v_mfma_f32_16x16x32_bf16 v[42:45], v[154:157], v[170:173], v[42:45]
	v_mfma_f32_16x16x32_bf16 v[38:41], v[162:165], v[170:173], v[38:41]
	v_mfma_f32_16x16x32_bf16 v[30:33], v[134:137], v[190:193], v[30:33]
	v_mfma_f32_16x16x32_bf16 v[26:29], v[142:145], v[190:193], v[26:29]
	v_mfma_f32_16x16x32_bf16 v[22:25], v[134:137], v[182:185], v[22:25]
	v_mfma_f32_16x16x32_bf16 v[18:21], v[142:145], v[182:185], v[18:21]
	v_mfma_f32_16x16x32_bf16 v[14:17], v[134:137], v[174:177], v[14:17]
	v_mfma_f32_16x16x32_bf16 v[10:13], v[142:145], v[174:177], v[10:13]
	v_mfma_f32_16x16x32_bf16 v[6:9], v[134:137], v[166:169], v[6:9]
	v_mfma_f32_16x16x32_bf16 v[2:5], v[142:145], v[166:169], v[2:5]
	v_mfma_f32_16x16x32_bf16 v[30:33], v[138:141], v[194:197], v[30:33]
	v_mfma_f32_16x16x32_bf16 v[26:29], v[146:149], v[194:197], v[26:29]
	v_mfma_f32_16x16x32_bf16 v[22:25], v[138:141], v[186:189], v[22:25]
	v_mfma_f32_16x16x32_bf16 v[18:21], v[146:149], v[186:189], v[18:21]
	v_mfma_f32_16x16x32_bf16 v[14:17], v[138:141], v[178:181], v[14:17]
	v_mfma_f32_16x16x32_bf16 v[10:13], v[146:149], v[178:181], v[10:13]
	v_mfma_f32_16x16x32_bf16 v[6:9], v[138:141], v[170:173], v[6:9]
	v_mfma_f32_16x16x32_bf16 v[2:5], v[146:149], v[170:173], v[2:5]
; #define PG8_STAGE(bufoff, gbase, voff) do { _Pragma("unroll") for (int _i = 0; _i < 2; ++_i) \
;         __builtin_amdgcn_global_load_lds((const unsigned*)((const char*)(gbase) + (voff)[_i]), (LAS unsigned*)(lds + (bufoff) + ldsw + _i * 8192), 16, 0, 0); } while (0)
; #define PG8_LDA(dst, b, h) do { _Pragma("unroll") for (int m = 0; m < 4; ++m) _Pragma("unroll") for (int k = 0; k < 2; ++k) dst[m][k] = *(const LAS bf16x8*)(lds + PG8_SA(b, h) + aoff + m * 2048 + k * 1024); } while (0)
; #define PG8_LDB(dst, b, h) do { _Pragma("unroll") for (int n = 0; n < 2; ++n) _Pragma("unroll") for (int k = 0; k < 2; ++k) dst[n][k] = *(const LAS bf16x8*)(lds + PG8_SB(b, h) + boff + n * 2048 + k * 1024); } while (0)
; #define PG8_MMA(ai, bj, At, Bt) do { __builtin_amdgcn_s_setprio(1); _Pragma("unroll") for (int m = 0; m < 4; ++m) _Pragma("unroll") for (int n = 0; n < 2; ++n) _Pragma("unroll") for (int k = 0; k < 2; ++k) \
;         acc[ai][bj][m][n] = __builtin_amdgcn_mfma_f32_16x16x32_bf16(Bt[n][k], At[m][k], acc[ai][bj][m][n], 0, 0, 0); __builtin_amdgcn_s_setprio(0); } while (0)
; #define PG8_WAIT_V(n) asm volatile("s_waitcnt vmcnt(" #n ")" ::: "memory")
; #define PG8_WAIT_L(n) asm volatile("s_waitcnt lgkmcnt(" #n ")" ::: "memory")
; #define PG8_BAR __builtin_amdgcn_s_barrier()
; #define PG8_SCHED __builtin_amdgcn_sched_barrier(0)
; #define PG8_STAGE(bufoff, gbase, voff) do { _Pragma("unroll") for (int _i = 0; _i < 2; ++_i) \
;         __builtin_amdgcn_global_load_lds((const unsigned*)((const char*)(gbase) + (voff)[_i]), (LAS unsigned*)(lds + (bufoff) + ldsw + _i * 8192), 16, 0, 0); } while (0)
; #define PG8_BAR __builtin_amdgcn_s_barrier()
; template <class Epi, class Sched>
; __device__ __forceinline__ void gemm_phase_gather(LAS unsigned char* lds, const int K, const Sched& S, const Epi& E, const char* Ag, const int* list, const LAS int* seg) {
;     ...
;             PG8_LDB(B0, 1, 0); PG8_LDB(B1, 1, 1); PG8_SCHED; PG8_LDA(At, 1, 0); PG8_STAGE(PG8_SA(0, 1), a2, x1);
;             PG8_WAIT_V(8); PG8_WAIT_L(0); PG8_BAR; PG8_MMA(0, 0, At, B0); PG8_MMA(0, 1, At, B1); PG8_BAR; PG8_SCHED;
;             PG8_LDA(At, 1, 1); PG8_STAGE(PG8_SB(1, 0), b3, voffB); PG8_STAGE(PG8_SB(1, 1), b3 + hstep, voffB); PG8_STAGE(PG8_SA(1, 0), a3, x0);
;             PG8_WAIT_V(8); PG8_WAIT_L(0); PG8_BAR; if (hi_on) { PG8_MMA(1, 0, At, B0); PG8_MMA(1, 1, At, B1); } PG8_BAR; PG8_SCHED;
;         }
.LBB0_1037:
	v_mov_b32_e32 v223, v35
	v_lshl_add_u64 v[230:231], s[40:41], 0, v[34:35]
	v_lshl_add_u64 v[222:223], s[40:41], 0, v[222:223]
	v_cndmask_b32_e64 v34, v210, v229, s[6:7]
	v_cndmask_b32_e64 v211, v214, v249, s[6:7]
	s_barrier
	s_add_i32 s6, 0, 0x18000
	s_add_i32 s33, 0, 0x1c000
	v_add_u32_e32 v134, s6, v248
	v_add_u32_e32 v146, s33, v248
	ds_read_b128 v[150:153], v134
	ds_read_b128 v[154:157], v134 offset:1024
	ds_read_b128 v[158:161], v134 offset:2048
	ds_read_b128 v[162:165], v134 offset:3072
	ds_read_b128 v[134:137], v146
	ds_read_b128 v[138:141], v146 offset:1024
	ds_read_b128 v[142:145], v146 offset:2048
	ds_read_b128 v[146:149], v146 offset:3072
	s_mov_b32 m0, s45
	s_waitcnt lgkmcnt(0)
	ds_read_b128 v[166:169], v213 offset:32768
	ds_read_b128 v[170:173], v213 offset:33792
	ds_read_b128 v[174:177], v213 offset:34816
	ds_read_b128 v[178:181], v213 offset:35840
	ds_read_b128 v[182:185], v213 offset:36864
	ds_read_b128 v[186:189], v213 offset:37888
	ds_read_b128 v[190:193], v213 offset:38912
	ds_read_b128 v[194:197], v213 offset:39936
	global_load_lds_dwordx4 v34, s[40:41]
	s_mov_b32 m0, s46
	s_nop 0
	global_load_lds_dwordx4 v211, s[40:41]
	s_waitcnt vmcnt(8)
	s_waitcnt lgkmcnt(0)
	s_barrier
	s_waitcnt lgkmcnt(0)
	v_mfma_f32_16x16x32_bf16 v[74:77], v[150:153], v[166:169], v[74:77]
	v_mfma_f32_16x16x32_bf16 v[130:133], v[158:161], v[166:169], v[130:133]
	v_mfma_f32_16x16x32_bf16 v[126:129], v[150:153], v[174:177], v[126:129]
	v_mfma_f32_16x16x32_bf16 v[122:125], v[158:161], v[174:177], v[122:125]
	v_mfma_f32_16x16x32_bf16 v[118:121], v[150:153], v[182:185], v[118:121]
	v_mfma_f32_16x16x32_bf16 v[114:117], v[158:161], v[182:185], v[114:117]
	v_mfma_f32_16x16x32_bf16 v[110:113], v[150:153], v[190:193], v[110:113]
	v_mfma_f32_16x16x32_bf16 v[106:109], v[158:161], v[190:193], v[106:109]
	v_mfma_f32_16x16x32_bf16 v[74:77], v[154:157], v[170:173], v[74:77]
	v_mfma_f32_16x16x32_bf16 v[130:133], v[162:165], v[170:173], v[130:133]
	v_mfma_f32_16x16x32_bf16 v[126:129], v[154:157], v[178:181], v[126:129]
	v_mfma_f32_16x16x32_bf16 v[122:125], v[162:165], v[178:181], v[122:125]
	v_mfma_f32_16x16x32_bf16 v[118:121], v[154:157], v[186:189], v[118:121]
	v_mfma_f32_16x16x32_bf16 v[114:117], v[162:165], v[186:189], v[114:117]
	v_mfma_f32_16x16x32_bf16 v[110:113], v[154:157], v[194:197], v[110:113]
	v_mfma_f32_16x16x32_bf16 v[106:109], v[162:165], v[194:197], v[106:109]
	v_mfma_f32_16x16x32_bf16 v[102:105], v[134:137], v[166:169], v[102:105]
	v_mfma_f32_16x16x32_bf16 v[98:101], v[142:145], v[166:169], v[98:101]
	v_mfma_f32_16x16x32_bf16 v[94:97], v[134:137], v[174:177], v[94:97]
	v_mfma_f32_16x16x32_bf16 v[90:93], v[142:145], v[174:177], v[90:93]
	v_mfma_f32_16x16x32_bf16 v[86:89], v[134:137], v[182:185], v[86:89]
	v_mfma_f32_16x16x32_bf16 v[82:85], v[142:145], v[182:185], v[82:85]
	v_mfma_f32_16x16x32_bf16 v[78:81], v[134:137], v[190:193], v[78:81]
	v_mfma_f32_16x16x32_bf16 v[70:73], v[142:145], v[190:193], v[70:73]
	v_mfma_f32_16x16x32_bf16 v[102:105], v[138:141], v[170:173], v[102:105]
	v_mfma_f32_16x16x32_bf16 v[98:101], v[146:149], v[170:173], v[98:101]
	v_mfma_f32_16x16x32_bf16 v[94:97], v[138:141], v[178:181], v[94:97]
	v_mfma_f32_16x16x32_bf16 v[90:93], v[146:149], v[178:181], v[90:93]
	v_mfma_f32_16x16x32_bf16 v[86:89], v[138:141], v[186:189], v[86:89]
	v_mfma_f32_16x16x32_bf16 v[82:85], v[146:149], v[186:189], v[82:85]
	v_mfma_f32_16x16x32_bf16 v[78:81], v[138:141], v[194:197], v[78:81]
	v_mfma_f32_16x16x32_bf16 v[70:73], v[146:149], v[194:197], v[70:73]
	s_barrier
	s_add_i32 s6, s6, s13
	v_lshl_add_u64 v[218:219], v[218:219], 0, s[88:89]
	s_mov_b32 m0, s6
	ds_read_b128 v[190:193], v213 offset:49152
	ds_read_b128 v[194:197], v213 offset:50176
	ds_read_b128 v[182:185], v213 offset:51200
	ds_read_b128 v[186:189], v213 offset:52224
	ds_read_b128 v[174:177], v213 offset:53248
	ds_read_b128 v[178:181], v213 offset:54272
	ds_read_b128 v[166:169], v213 offset:55296
	ds_read_b128 v[170:173], v213 offset:56320
	global_load_lds_dwordx4 v[218:219], off
	s_add_i32 m0, s6, 0x2000
	s_add_u32 s6, s38, 0x40080
	v_lshl_add_u64 v[218:219], v[220:221], 0, s[88:89]
	s_addc_u32 s7, s39, 0
	s_add_i32 s33, s33, s13
	global_load_lds_dwordx4 v[218:219], off
	v_lshl_add_u64 v[218:219], s[6:7], 0, v[204:205]
	s_mov_b32 m0, s33
	s_and_b64 vcc, exec, s[8:9]
	global_load_lds_dwordx4 v[218:219], off
	v_lshl_add_u64 v[218:219], s[6:7], 0, v[206:207]
	s_add_i32 m0, s33, 0x2000
	s_nop 0
	global_load_lds_dwordx4 v[218:219], off
	v_lshl_add_u64 v[218:219], v[230:231], 0, s[88:89]
	s_mov_b32 m0, s47
	s_nop 0
	global_load_lds_dwordx4 v[218:219], off
	v_lshl_add_u64 v[218:219], v[222:223], 0, s[88:89]
	s_mov_b32 m0, s48
	s_nop 0
	global_load_lds_dwordx4 v[218:219], off
	s_waitcnt vmcnt(8)
	s_waitcnt lgkmcnt(0)
	s_barrier
	s_cbranch_vccnz .LBB0_1034
	s_waitcnt lgkmcnt(0)
	v_mfma_f32_16x16x32_bf16 v[66:69], v[150:153], v[190:193], v[66:69]
	v_mfma_f32_16x16x32_bf16 v[62:65], v[158:161], v[190:193], v[62:65]
	v_mfma_f32_16x16x32_bf16 v[58:61], v[150:153], v[182:185], v[58:61]
	v_mfma_f32_16x16x32_bf16 v[54:57], v[158:161], v[182:185], v[54:57]
	v_mfma_f32_16x16x32_bf16 v[50:53], v[150:153], v[174:177], v[50:53]
	v_mfma_f32_16x16x32_bf16 v[46:49], v[158:161], v[174:177], v[46:49]
	v_mfma_f32_16x16x32_bf16 v[42:45], v[150:153], v[166:169], v[42:45]
	v_mfma_f32_16x16x32_bf16 v[38:41], v[158:161], v[166:169], v[38:41]
	v_mfma_f32_16x16x32_bf16 v[66:69], v[154:157], v[194:197], v[66:69]
	v_mfma_f32_16x16x32_bf16 v[62:65], v[162:165], v[194:197], v[62:65]
	v_mfma_f32_16x16x32_bf16 v[58:61], v[154:157], v[186:189], v[58:61]
	v_mfma_f32_16x16x32_bf16 v[54:57], v[162:165], v[186:189], v[54:57]
	v_mfma_f32_16x16x32_bf16 v[50:53], v[154:157], v[178:181], v[50:53]
	v_mfma_f32_16x16x32_bf16 v[46:49], v[162:165], v[178:181], v[46:49]
	v_mfma_f32_16x16x32_bf16 v[42:45], v[154:157], v[170:173], v[42:45]
	v_mfma_f32_16x16x32_bf16 v[38:41], v[162:165], v[170:173], v[38:41]
	v_mfma_f32_16x16x32_bf16 v[30:33], v[134:137], v[190:193], v[30:33]
	v_mfma_f32_16x16x32_bf16 v[26:29], v[142:145], v[190:193], v[26:29]
	v_mfma_f32_16x16x32_bf16 v[22:25], v[134:137], v[182:185], v[22:25]
	v_mfma_f32_16x16x32_bf16 v[18:21], v[142:145], v[182:185], v[18:21]
	v_mfma_f32_16x16x32_bf16 v[14:17], v[134:137], v[174:177], v[14:17]
	v_mfma_f32_16x16x32_bf16 v[10:13], v[142:145], v[174:177], v[10:13]
	v_mfma_f32_16x16x32_bf16 v[6:9], v[134:137], v[166:169], v[6:9]
	v_mfma_f32_16x16x32_bf16 v[2:5], v[142:145], v[166:169], v[2:5]
	v_mfma_f32_16x16x32_bf16 v[30:33], v[138:141], v[194:197], v[30:33]
	v_mfma_f32_16x16x32_bf16 v[26:29], v[146:149], v[194:197], v[26:29]
	v_mfma_f32_16x16x32_bf16 v[22:25], v[138:141], v[186:189], v[22:25]
	v_mfma_f32_16x16x32_bf16 v[18:21], v[146:149], v[186:189], v[18:21]
	v_mfma_f32_16x16x32_bf16 v[14:17], v[138:141], v[178:181], v[14:17]
	v_mfma_f32_16x16x32_bf16 v[10:13], v[146:149], v[178:181], v[10:13]
	v_mfma_f32_16x16x32_bf16 v[6:9], v[138:141], v[170:173], v[6:9]
	v_mfma_f32_16x16x32_bf16 v[2:5], v[146:149], v[170:173], v[2:5]
	s_branch .LBB0_1034

; #define PG8_STAGE(bufoff, gbase, voff) do { _Pragma("unroll") for (int _i = 0; _i < 2; ++_i) \
;         __builtin_amdgcn_global_load_lds((const unsigned*)((const char*)(gbase) + (voff)[_i]), (LAS unsigned*)(lds + (bufoff) + ldsw + _i * 8192), 16, 0, 0); } while (0)
; #define PG8_LDA(dst, b, h) do { _Pragma("unroll") for (int m = 0; m < 4; ++m) _Pragma("unroll") for (int k = 0; k < 2; ++k) dst[m][k] = *(const LAS bf16x8*)(lds + PG8_SA(b, h) + aoff + m * 2048 + k * 1024); } while (0)
; #define PG8_LDB(dst, b, h) do { _Pragma("unroll") for (int n = 0; n < 2; ++n) _Pragma("unroll") for (int k = 0; k < 2; ++k) dst[n][k] = *(const LAS bf16x8*)(lds + PG8_SB(b, h) + boff + n * 2048 + k * 1024); } while (0)
; #define PG8_MMA(ai, bj, At, Bt) do { __builtin_amdgcn_s_setprio(1); _Pragma("unroll") for (int m = 0; m < 4; ++m) _Pragma("unroll") for (int n = 0; n < 2; ++n) _Pragma("unroll") for (int k = 0; k < 2; ++k) \
;         acc[ai][bj][m][n] = __builtin_amdgcn_mfma_f32_16x16x32_bf16(Bt[n][k], At[m][k], acc[ai][bj][m][n], 0, 0, 0); __builtin_amdgcn_s_setprio(0); } while (0)
; #define PG8_WAIT_V(n) asm volatile("s_waitcnt vmcnt(" #n ")" ::: "memory")
; #define PG8_WAIT_L(n) asm volatile("s_waitcnt lgkmcnt(" #n ")" ::: "memory")
; #define PG8_BAR __builtin_amdgcn_s_barrier()
; #define PG8_SCHED __builtin_amdgcn_sched_barrier(0)
; #define PG8_WAIT_V(n) asm volatile("s_waitcnt vmcnt(" #n ")" ::: "memory")
; #define PG8_WAIT_L(n) asm volatile("s_waitcnt lgkmcnt(" #n ")" ::: "memory")
;     ...
;         for (int t = 0; t < nt; t += 2) {
;             const bool last = (t == nt - 2);
;             const char* a1 = cA + (size_t)(t + 1) * kstepA;
;             const char* a2 = last ? nA : cA + (size_t)(t + 2) * kstepA; const char* b2 = last ? nB : cB + (size_t)(t + 2) * kstep;
;             const char* a3 = a2 + kstepA; const char* b3 = b2 + kstep;
;             PG8_LDB(B0, 0, 0); PG8_LDB(B1, 0, 1); PG8_SCHED; PG8_LDA(At, 0, 0); PG8_STAGE(PG8_SA(1, 1), a1 + hstepA, voffA);
;             PG8_WAIT_V(8); PG8_WAIT_L(0); PG8_BAR; PG8_MMA(0, 0, At, B0); PG8_MMA(0, 1, At, B1); PG8_BAR; PG8_SCHED;
;             PG8_LDA(At, 0, 1); PG8_STAGE(PG8_SB(0, 0), b2, voffB); PG8_STAGE(PG8_SB(0, 1), b2 + hstep, voffB); PG8_STAGE(PG8_SA(0, 0), a2, voffA);
;             PG8_WAIT_V(8); PG8_WAIT_L(0); PG8_BAR; if (hi_on) { PG8_MMA(1, 0, At, B0); PG8_MMA(1, 1, At, B1); } PG8_BAR; PG8_SCHED;
.LBB0_1294:
	s_add_u32 s8, s14, s34
	s_addc_u32 s9, s15, s35
	s_add_u32 s8, s8, 0x100
	s_addc_u32 s9, s9, 0
	s_add_u32 s33, s55, s34
	s_addc_u32 s36, s66, s35
	s_add_i32 s58, 0, 0x10000
	s_cmpk_eq_i32 s34, 0x300
	s_cselect_b32 s39, s29, s9
	s_cselect_b32 s38, s28, s8
	v_add_u32_e32 v34, s58, v227
	s_cselect_b32 s37, s27, s36
	s_cselect_b32 s36, s26, s33
	s_add_i32 s33, 0, 0x14000
	ds_read_b128 v[150:153], v34
	ds_read_b128 v[154:157], v34 offset:1024
	ds_read_b128 v[158:161], v34 offset:2048
	ds_read_b128 v[162:165], v34 offset:3072
	v_add_u32_e32 v34, s33, v227
	ds_read_b128 v[134:137], v34
	ds_read_b128 v[138:141], v34 offset:1024
	ds_read_b128 v[142:145], v34 offset:2048
	ds_read_b128 v[146:149], v34 offset:3072
	v_lshl_add_u64 v[218:219], v[36:37], 0, s[34:35]
	s_add_i32 m0, s13, 0xc000
	s_waitcnt lgkmcnt(0)
	ds_read_b128 v[166:169], v245
	ds_read_b128 v[170:173], v245 offset:1024
	ds_read_b128 v[174:177], v245 offset:2048
	ds_read_b128 v[178:181], v245 offset:3072
	ds_read_b128 v[182:185], v245 offset:4096
	ds_read_b128 v[186:189], v245 offset:5120
	ds_read_b128 v[190:193], v245 offset:6144
	ds_read_b128 v[194:197], v245 offset:7168
	global_load_lds_dwordx4 v[218:219], off
	v_lshl_add_u64 v[218:219], v[216:217], 0, s[34:35]
	s_add_i32 m0, s13, 0xe000
	s_nop 0
	global_load_lds_dwordx4 v[218:219], off
	s_waitcnt vmcnt(8)
	s_waitcnt lgkmcnt(0)
	s_barrier
	s_waitcnt lgkmcnt(0)
	v_mfma_f32_16x16x32_bf16 v[130:133], v[150:153], v[166:169], v[130:133]
	v_mfma_f32_16x16x32_bf16 v[126:129], v[158:161], v[166:169], v[126:129]
	v_mfma_f32_16x16x32_bf16 v[122:125], v[150:153], v[174:177], v[122:125]
	v_mfma_f32_16x16x32_bf16 v[118:121], v[158:161], v[174:177], v[118:121]
	v_mfma_f32_16x16x32_bf16 v[114:117], v[150:153], v[182:185], v[114:117]
	v_mfma_f32_16x16x32_bf16 v[110:113], v[158:161], v[182:185], v[110:113]
	v_mfma_f32_16x16x32_bf16 v[106:109], v[150:153], v[190:193], v[106:109]
	v_mfma_f32_16x16x32_bf16 v[102:105], v[158:161], v[190:193], v[102:105]
	v_mfma_f32_16x16x32_bf16 v[130:133], v[154:157], v[170:173], v[130:133]
	v_mfma_f32_16x16x32_bf16 v[126:129], v[162:165], v[170:173], v[126:129]
	v_mfma_f32_16x16x32_bf16 v[122:125], v[154:157], v[178:181], v[122:125]
	v_mfma_f32_16x16x32_bf16 v[118:121], v[162:165], v[178:181], v[118:121]
	v_mfma_f32_16x16x32_bf16 v[114:117], v[154:157], v[186:189], v[114:117]
	v_mfma_f32_16x16x32_bf16 v[110:113], v[162:165], v[186:189], v[110:113]
	v_mfma_f32_16x16x32_bf16 v[106:109], v[154:157], v[194:197], v[106:109]
	v_mfma_f32_16x16x32_bf16 v[102:105], v[162:165], v[194:197], v[102:105]
	v_mfma_f32_16x16x32_bf16 v[98:101], v[134:137], v[166:169], v[98:101]
	v_mfma_f32_16x16x32_bf16 v[94:97], v[142:145], v[166:169], v[94:97]
	v_mfma_f32_16x16x32_bf16 v[90:93], v[134:137], v[174:177], v[90:93]
	v_mfma_f32_16x16x32_bf16 v[86:89], v[142:145], v[174:177], v[86:89]
	v_mfma_f32_16x16x32_bf16 v[82:85], v[134:137], v[182:185], v[82:85]
	v_mfma_f32_16x16x32_bf16 v[78:81], v[142:145], v[182:185], v[78:81]
	v_mfma_f32_16x16x32_bf16 v[74:77], v[134:137], v[190:193], v[74:77]
	v_mfma_f32_16x16x32_bf16 v[70:73], v[142:145], v[190:193], v[70:73]
	v_mfma_f32_16x16x32_bf16 v[98:101], v[138:141], v[170:173], v[98:101]
	v_mfma_f32_16x16x32_bf16 v[94:97], v[146:149], v[170:173], v[94:97]
	v_mfma_f32_16x16x32_bf16 v[90:93], v[138:141], v[178:181], v[90:93]
	v_mfma_f32_16x16x32_bf16 v[86:89], v[146:149], v[178:181], v[86:89]
	v_mfma_f32_16x16x32_bf16 v[82:85], v[138:141], v[186:189], v[82:85]
	v_mfma_f32_16x16x32_bf16 v[78:81], v[146:149], v[186:189], v[78:81]
	v_mfma_f32_16x16x32_bf16 v[74:77], v[138:141], v[194:197], v[74:77]
	v_mfma_f32_16x16x32_bf16 v[70:73], v[146:149], v[194:197], v[70:73]
	s_barrier
	s_add_i32 s8, s58, s11
	v_lshl_add_u64 v[218:219], s[36:37], 0, v[206:207]
	s_mov_b32 m0, s8
	ds_read_b128 v[190:193], v245 offset:16384
	ds_read_b128 v[194:197], v245 offset:17408
	ds_read_b128 v[182:185], v245 offset:18432
	ds_read_b128 v[186:189], v245 offset:19456
	ds_read_b128 v[174:177], v245 offset:20480
	ds_read_b128 v[178:181], v245 offset:21504
	ds_read_b128 v[166:169], v245 offset:22528
	ds_read_b128 v[170:173], v245 offset:23552
	global_load_lds_dwordx4 v[218:219], off
	s_add_i32 m0, s8, 0x2000
	s_add_u32 s8, s36, 0x20000
	v_lshl_add_u64 v[220:221], s[36:37], 0, v[210:211]
	s_addc_u32 s9, s37, 0
	s_add_i32 s33, s33, s11
	global_load_lds_dwordx4 v[220:221], off
	v_lshl_add_u64 v[222:223], s[8:9], 0, v[206:207]
	s_mov_b32 m0, s33
	v_lshl_add_u64 v[224:225], s[38:39], 0, v[208:209]
	global_load_lds_dwordx4 v[222:223], off
	v_lshl_add_u64 v[222:223], s[8:9], 0, v[210:211]
	s_add_i32 m0, s33, 0x2000
	v_cndmask_b32_e64 v34, 0, 1, s[6:7]
	global_load_lds_dwordx4 v[222:223], off
	v_lshl_add_u64 v[222:223], s[38:39], 0, v[204:205]
	s_mov_b32 m0, s13
	v_cmp_ne_u32_e64 s[8:9], 1, v34
	global_load_lds_dwordx4 v[222:223], off
	s_mov_b32 m0, s43
	s_andn2_b64 vcc, exec, s[6:7]
	global_load_lds_dwordx4 v[224:225], off
	s_waitcnt vmcnt(8)
	s_waitcnt lgkmcnt(0)
	s_barrier
	s_cbranch_vccnz .LBB0_1296
; #define PG8_MMA(ai, bj, At, Bt) do { __builtin_amdgcn_s_setprio(1); _Pragma("unroll") for (int m = 0; m < 4; ++m) _Pragma("unroll") for (int n = 0; n < 2; ++n) _Pragma("unroll") for (int k = 0; k < 2; ++k) \
;         acc[ai][bj][m][n] = __builtin_amdgcn_mfma_f32_16x16x32_bf16(Bt[n][k], At[m][k], acc[ai][bj][m][n], 0, 0, 0); __builtin_amdgcn_s_setprio(0); } while (0)
; #define PG8_WAIT_V(n) asm volatile("s_waitcnt vmcnt(" #n ")" ::: "memory")
; #define PG8_WAIT_L(n) asm volatile("s_waitcnt lgkmcnt(" #n ")" ::: "memory")
; #define PG8_BAR __builtin_amdgcn_s_barrier()
; #define PG8_SCHED __builtin_amdgcn_sched_barrier(0)
; #define PG8_MMA(ai, bj, At, Bt) do { __builtin_amdgcn_s_setprio(1); _Pragma("unroll") for (int m = 0; m < 4; ++m) _Pragma("unroll") for (int n = 0; n < 2; ++n) _Pragma("unroll") for (int k = 0; k < 2; ++k) \
;         acc[ai][bj][m][n] = __builtin_amdgcn_mfma_f32_16x16x32_bf16(Bt[n][k], At[m][k], acc[ai][bj][m][n], 0, 0, 0); __builtin_amdgcn_s_setprio(0); } while (0)
; #define PG8_WAIT_V(n) asm volatile("s_waitcnt vmcnt(" #n ")" ::: "memory")
; #define PG8_WAIT_L(n) asm volatile("s_waitcnt lgkmcnt(" #n ")" ::: "memory")
; #define PG8_BAR __builtin_amdgcn_s_barrier()
; #define PG8_SCHED __builtin_amdgcn_sched_barrier(0)
;     ...
;             PG8_WAIT_V(8); PG8_WAIT_L(0); PG8_BAR; if (hi_on) { PG8_MMA(1, 0, At, B0); PG8_MMA(1, 1, At, B1); } PG8_BAR; PG8_SCHED;
	s_waitcnt lgkmcnt(0)
	v_mfma_f32_16x16x32_bf16 v[66:69], v[150:153], v[190:193], v[66:69]
	v_mfma_f32_16x16x32_bf16 v[62:65], v[158:161], v[190:193], v[62:65]
	v_mfma_f32_16x16x32_bf16 v[58:61], v[150:153], v[182:185], v[58:61]
	v_mfma_f32_16x16x32_bf16 v[54:57], v[158:161], v[182:185], v[54:57]
	v_mfma_f32_16x16x32_bf16 v[50:53], v[150:153], v[174:177], v[50:53]
	v_mfma_f32_16x16x32_bf16 v[46:49], v[158:161], v[174:177], v[46:49]
	v_mfma_f32_16x16x32_bf16 v[42:45], v[150:153], v[166:169], v[42:45]
	v_mfma_f32_16x16x32_bf16 v[38:41], v[158:161], v[166:169], v[38:41]
	v_mfma_f32_16x16x32_bf16 v[66:69], v[154:157], v[194:197], v[66:69]
	v_mfma_f32_16x16x32_bf16 v[62:65], v[162:165], v[194:197], v[62:65]
	v_mfma_f32_16x16x32_bf16 v[58:61], v[154:157], v[186:189], v[58:61]
	v_mfma_f32_16x16x32_bf16 v[54:57], v[162:165], v[186:189], v[54:57]
	v_mfma_f32_16x16x32_bf16 v[50:53], v[154:157], v[178:181], v[50:53]
	v_mfma_f32_16x16x32_bf16 v[46:49], v[162:165], v[178:181], v[46:49]
	v_mfma_f32_16x16x32_bf16 v[42:45], v[154:157], v[170:173], v[42:45]
	v_mfma_f32_16x16x32_bf16 v[38:41], v[162:165], v[170:173], v[38:41]
	v_mfma_f32_16x16x32_bf16 v[30:33], v[134:137], v[190:193], v[30:33]
	v_mfma_f32_16x16x32_bf16 v[26:29], v[142:145], v[190:193], v[26:29]
	v_mfma_f32_16x16x32_bf16 v[22:25], v[134:137], v[182:185], v[22:25]
	v_mfma_f32_16x16x32_bf16 v[18:21], v[142:145], v[182:185], v[18:21]
	v_mfma_f32_16x16x32_bf16 v[14:17], v[134:137], v[174:177], v[14:17]
	v_mfma_f32_16x16x32_bf16 v[10:13], v[142:145], v[174:177], v[10:13]
	v_mfma_f32_16x16x32_bf16 v[6:9], v[134:137], v[166:169], v[6:9]
	v_mfma_f32_16x16x32_bf16 v[2:5], v[142:145], v[166:169], v[2:5]
	v_mfma_f32_16x16x32_bf16 v[30:33], v[138:141], v[194:197], v[30:33]
	v_mfma_f32_16x16x32_bf16 v[26:29], v[146:149], v[194:197], v[26:29]
	v_mfma_f32_16x16x32_bf16 v[22:25], v[138:141], v[186:189], v[22:25]
	v_mfma_f32_16x16x32_bf16 v[18:21], v[146:149], v[186:189], v[18:21]
	v_mfma_f32_16x16x32_bf16 v[14:17], v[138:141], v[178:181], v[14:17]
	v_mfma_f32_16x16x32_bf16 v[10:13], v[146:149], v[178:181], v[10:13]
	v_mfma_f32_16x16x32_bf16 v[6:9], v[138:141], v[170:173], v[6:9]
	v_mfma_f32_16x16x32_bf16 v[2:5], v[146:149], v[170:173], v[2:5]
; #define PG8_STAGE(bufoff, gbase, voff) do { _Pragma("unroll") for (int _i = 0; _i < 2; ++_i) \
;         __builtin_amdgcn_global_load_lds((const unsigned*)((const char*)(gbase) + (voff)[_i]), (LAS unsigned*)(lds + (bufoff) + ldsw + _i * 8192), 16, 0, 0); } while (0)
; #define PG8_LDA(dst, b, h) do { _Pragma("unroll") for (int m = 0; m < 4; ++m) _Pragma("unroll") for (int k = 0; k < 2; ++k) dst[m][k] = *(const LAS bf16x8*)(lds + PG8_SA(b, h) + aoff + m * 2048 + k * 1024); } while (0)
; #define PG8_LDB(dst, b, h) do { _Pragma("unroll") for (int n = 0; n < 2; ++n) _Pragma("unroll") for (int k = 0; k < 2; ++k) dst[n][k] = *(const LAS bf16x8*)(lds + PG8_SB(b, h) + boff + n * 2048 + k * 1024); } while (0)
; #define PG8_MMA(ai, bj, At, Bt) do { __builtin_amdgcn_s_setprio(1); _Pragma("unroll") for (int m = 0; m < 4; ++m) _Pragma("unroll") for (int n = 0; n < 2; ++n) _Pragma("unroll") for (int k = 0; k < 2; ++k) \
;         acc[ai][bj][m][n] = __builtin_amdgcn_mfma_f32_16x16x32_bf16(Bt[n][k], At[m][k], acc[ai][bj][m][n], 0, 0, 0); __builtin_amdgcn_s_setprio(0); } while (0)
; #define PG8_WAIT_V(n) asm volatile("s_waitcnt vmcnt(" #n ")" ::: "memory")
; #define PG8_WAIT_L(n) asm volatile("s_waitcnt lgkmcnt(" #n ")" ::: "memory")
; #define PG8_BAR __builtin_amdgcn_s_barrier()
; #define PG8_SCHED __builtin_amdgcn_sched_barrier(0)
; #define PG8_STAGE(bufoff, gbase, voff) do { _Pragma("unroll") for (int _i = 0; _i < 2; ++_i) \
;         __builtin_amdgcn_global_load_lds((const unsigned*)((const char*)(gbase) + (voff)[_i]), (LAS unsigned*)(lds + (bufoff) + ldsw + _i * 8192), 16, 0, 0); } while (0)
; #define PG8_LDA(dst, b, h) do { _Pragma("unroll") for (int m = 0; m < 4; ++m) _Pragma("unroll") for (int k = 0; k < 2; ++k) dst[m][k] = *(const LAS bf16x8*)(lds + PG8_SA(b, h) + aoff + m * 2048 + k * 1024); } while (0)
;     ...
;             PG8_LDB(B0, 1, 0); PG8_LDB(B1, 1, 1); PG8_SCHED; PG8_LDA(At, 1, 0); PG8_STAGE(PG8_SA(0, 1), a2 + hstepA, voffA);
;             PG8_WAIT_V(8); PG8_WAIT_L(0); PG8_BAR; PG8_MMA(0, 0, At, B0); PG8_MMA(0, 1, At, B1); PG8_BAR; PG8_SCHED;
;             PG8_LDA(At, 1, 1); PG8_STAGE(PG8_SB(1, 0), b3, voffB); PG8_STAGE(PG8_SB(1, 1), b3 + hstep, voffB); PG8_STAGE(PG8_SA(1, 0), a3, voffA);
;             PG8_WAIT_V(8); PG8_WAIT_L(0); PG8_BAR; if (hi_on) { PG8_MMA(1, 0, At, B0); PG8_MMA(1, 1, At, B1); } PG8_BAR; PG8_SCHED;
;         }
.LBB0_1296:
	s_barrier
	s_add_i32 s33, 0, 0x18000
	v_add_u32_e32 v34, s33, v227
	s_add_i32 s58, 0, 0x1c000
	ds_read_b128 v[150:153], v34
	ds_read_b128 v[154:157], v34 offset:1024
	ds_read_b128 v[158:161], v34 offset:2048
	ds_read_b128 v[162:165], v34 offset:3072
	v_add_u32_e32 v34, s58, v227
	ds_read_b128 v[134:137], v34
	ds_read_b128 v[138:141], v34 offset:1024
	ds_read_b128 v[142:145], v34 offset:2048
	ds_read_b128 v[146:149], v34 offset:3072
	s_add_u32 s38, s38, 0x20000
	s_addc_u32 s39, s39, 0
	s_mov_b32 m0, s44
	v_lshl_add_u64 v[230:231], s[38:39], 0, v[204:205]
	s_waitcnt lgkmcnt(0)
	ds_read_b128 v[166:169], v245 offset:32768
	ds_read_b128 v[170:173], v245 offset:33792
	ds_read_b128 v[174:177], v245 offset:34816
	ds_read_b128 v[178:181], v245 offset:35840
	ds_read_b128 v[182:185], v245 offset:36864
	ds_read_b128 v[186:189], v245 offset:37888
	ds_read_b128 v[190:193], v245 offset:38912
	ds_read_b128 v[194:197], v245 offset:39936
	global_load_lds_dwordx4 v[230:231], off
	v_lshl_add_u64 v[230:231], s[38:39], 0, v[208:209]
	s_mov_b32 m0, s45
	s_nop 0
	global_load_lds_dwordx4 v[230:231], off
	s_waitcnt vmcnt(8)
	s_waitcnt lgkmcnt(0)
	s_barrier
	s_waitcnt lgkmcnt(0)
	v_mfma_f32_16x16x32_bf16 v[130:133], v[150:153], v[166:169], v[130:133]
	v_mfma_f32_16x16x32_bf16 v[126:129], v[158:161], v[166:169], v[126:129]
	v_mfma_f32_16x16x32_bf16 v[122:125], v[150:153], v[174:177], v[122:125]
	v_mfma_f32_16x16x32_bf16 v[118:121], v[158:161], v[174:177], v[118:121]
	v_mfma_f32_16x16x32_bf16 v[114:117], v[150:153], v[182:185], v[114:117]
	v_mfma_f32_16x16x32_bf16 v[110:113], v[158:161], v[182:185], v[110:113]
	v_mfma_f32_16x16x32_bf16 v[106:109], v[150:153], v[190:193], v[106:109]
	v_mfma_f32_16x16x32_bf16 v[102:105], v[158:161], v[190:193], v[102:105]
	v_mfma_f32_16x16x32_bf16 v[130:133], v[154:157], v[170:173], v[130:133]
	v_mfma_f32_16x16x32_bf16 v[126:129], v[162:165], v[170:173], v[126:129]
	v_mfma_f32_16x16x32_bf16 v[122:125], v[154:157], v[178:181], v[122:125]
	v_mfma_f32_16x16x32_bf16 v[118:121], v[162:165], v[178:181], v[118:121]
	v_mfma_f32_16x16x32_bf16 v[114:117], v[154:157], v[186:189], v[114:117]
	v_mfma_f32_16x16x32_bf16 v[110:113], v[162:165], v[186:189], v[110:113]
	v_mfma_f32_16x16x32_bf16 v[106:109], v[154:157], v[194:197], v[106:109]
	v_mfma_f32_16x16x32_bf16 v[102:105], v[162:165], v[194:197], v[102:105]
	v_mfma_f32_16x16x32_bf16 v[98:101], v[134:137], v[166:169], v[98:101]
	v_mfma_f32_16x16x32_bf16 v[94:97], v[142:145], v[166:169], v[94:97]
	v_mfma_f32_16x16x32_bf16 v[90:93], v[134:137], v[174:177], v[90:93]
	v_mfma_f32_16x16x32_bf16 v[86:89], v[142:145], v[174:177], v[86:89]
	v_mfma_f32_16x16x32_bf16 v[82:85], v[134:137], v[182:185], v[82:85]
	v_mfma_f32_16x16x32_bf16 v[78:81], v[142:145], v[182:185], v[78:81]
	v_mfma_f32_16x16x32_bf16 v[74:77], v[134:137], v[190:193], v[74:77]
	v_mfma_f32_16x16x32_bf16 v[70:73], v[142:145], v[190:193], v[70:73]
	v_mfma_f32_16x16x32_bf16 v[98:101], v[138:141], v[170:173], v[98:101]
	v_mfma_f32_16x16x32_bf16 v[94:97], v[146:149], v[170:173], v[94:97]
	v_mfma_f32_16x16x32_bf16 v[90:93], v[138:141], v[178:181], v[90:93]
	v_mfma_f32_16x16x32_bf16 v[86:89], v[146:149], v[178:181], v[86:89]
	v_mfma_f32_16x16x32_bf16 v[82:85], v[138:141], v[186:189], v[82:85]
	v_mfma_f32_16x16x32_bf16 v[78:81], v[146:149], v[186:189], v[78:81]
	v_mfma_f32_16x16x32_bf16 v[74:77], v[138:141], v[194:197], v[74:77]
	v_mfma_f32_16x16x32_bf16 v[70:73], v[146:149], v[194:197], v[70:73]
	s_barrier
	s_add_i32 s33, s33, s11
	v_lshl_add_u64 v[218:219], v[218:219], 0, s[88:89]
	s_mov_b32 m0, s33
	ds_read_b128 v[190:193], v245 offset:49152
	ds_read_b128 v[194:197], v245 offset:50176
	ds_read_b128 v[182:185], v245 offset:51200
	ds_read_b128 v[186:189], v245 offset:52224
	ds_read_b128 v[174:177], v245 offset:53248
	ds_read_b128 v[178:181], v245 offset:54272
	ds_read_b128 v[166:169], v245 offset:55296
	ds_read_b128 v[170:173], v245 offset:56320
	global_load_lds_dwordx4 v[218:219], off
	s_add_i32 m0, s33, 0x2000
	s_add_u32 s36, s36, 0x20080
	v_lshl_add_u64 v[218:219], v[220:221], 0, s[88:89]
	s_addc_u32 s37, s37, 0
	s_add_i32 s33, s58, s11
	global_load_lds_dwordx4 v[218:219], off
	v_lshl_add_u64 v[218:219], s[36:37], 0, v[206:207]
	s_mov_b32 m0, s33
	s_and_b64 vcc, exec, s[8:9]
	global_load_lds_dwordx4 v[218:219], off
	v_lshl_add_u64 v[218:219], s[36:37], 0, v[210:211]
	s_add_i32 m0, s33, 0x2000
	s_nop 0
	global_load_lds_dwordx4 v[218:219], off
	v_lshl_add_u64 v[218:219], v[222:223], 0, s[88:89]
	s_mov_b32 m0, s46
	s_nop 0
	global_load_lds_dwordx4 v[218:219], off
	v_lshl_add_u64 v[218:219], v[224:225], 0, s[88:89]
	s_mov_b32 m0, s47
	s_nop 0
	global_load_lds_dwordx4 v[218:219], off
	s_waitcnt vmcnt(8)
	s_waitcnt lgkmcnt(0)
	s_barrier
	s_cbranch_vccnz .LBB0_1293
	s_waitcnt lgkmcnt(0)
	v_mfma_f32_16x16x32_bf16 v[66:69], v[150:153], v[190:193], v[66:69]
	v_mfma_f32_16x16x32_bf16 v[62:65], v[158:161], v[190:193], v[62:65]
	v_mfma_f32_16x16x32_bf16 v[58:61], v[150:153], v[182:185], v[58:61]
	v_mfma_f32_16x16x32_bf16 v[54:57], v[158:161], v[182:185], v[54:57]
	v_mfma_f32_16x16x32_bf16 v[50:53], v[150:153], v[174:177], v[50:53]
	v_mfma_f32_16x16x32_bf16 v[46:49], v[158:161], v[174:177], v[46:49]
	v_mfma_f32_16x16x32_bf16 v[42:45], v[150:153], v[166:169], v[42:45]
	v_mfma_f32_16x16x32_bf16 v[38:41], v[158:161], v[166:169], v[38:41]
	v_mfma_f32_16x16x32_bf16 v[66:69], v[154:157], v[194:197], v[66:69]
	v_mfma_f32_16x16x32_bf16 v[62:65], v[162:165], v[194:197], v[62:65]
	v_mfma_f32_16x16x32_bf16 v[58:61], v[154:157], v[186:189], v[58:61]
	v_mfma_f32_16x16x32_bf16 v[54:57], v[162:165], v[186:189], v[54:57]
	v_mfma_f32_16x16x32_bf16 v[50:53], v[154:157], v[178:181], v[50:53]
	v_mfma_f32_16x16x32_bf16 v[46:49], v[162:165], v[178:181], v[46:49]
	v_mfma_f32_16x16x32_bf16 v[42:45], v[154:157], v[170:173], v[42:45]
	v_mfma_f32_16x16x32_bf16 v[38:41], v[162:165], v[170:173], v[38:41]
	v_mfma_f32_16x16x32_bf16 v[30:33], v[134:137], v[190:193], v[30:33]
	v_mfma_f32_16x16x32_bf16 v[26:29], v[142:145], v[190:193], v[26:29]
	v_mfma_f32_16x16x32_bf16 v[22:25], v[134:137], v[182:185], v[22:25]
	v_mfma_f32_16x16x32_bf16 v[18:21], v[142:145], v[182:185], v[18:21]
	v_mfma_f32_16x16x32_bf16 v[14:17], v[134:137], v[174:177], v[14:17]
	v_mfma_f32_16x16x32_bf16 v[10:13], v[142:145], v[174:177], v[10:13]
	v_mfma_f32_16x16x32_bf16 v[6:9], v[134:137], v[166:169], v[6:9]
	v_mfma_f32_16x16x32_bf16 v[2:5], v[142:145], v[166:169], v[2:5]
	v_mfma_f32_16x16x32_bf16 v[30:33], v[138:141], v[194:197], v[30:33]
	v_mfma_f32_16x16x32_bf16 v[26:29], v[146:149], v[194:197], v[26:29]
	v_mfma_f32_16x16x32_bf16 v[22:25], v[138:141], v[186:189], v[22:25]
	v_mfma_f32_16x16x32_bf16 v[18:21], v[146:149], v[186:189], v[18:21]
	v_mfma_f32_16x16x32_bf16 v[14:17], v[138:141], v[178:181], v[14:17]
	v_mfma_f32_16x16x32_bf16 v[10:13], v[146:149], v[178:181], v[10:13]
	v_mfma_f32_16x16x32_bf16 v[6:9], v[138:141], v[170:173], v[6:9]
	v_mfma_f32_16x16x32_bf16 v[2:5], v[146:149], v[170:173], v[2:5]
	s_branch .LBB0_1293
